# fp8 MFMAs whose block scales are both 1.0 issued as the unscaled v_mfma_f32_*_f8f6f4 form (same e4m3 operands, same f32 accumulate, bit-identical results; no scale-load prefix)
# speedup vs baseline: 1.0155x; 1.0121x over previous
.LBB0_242:
	v_mov_b32_e32 v163, v0
	v_mov_b32_e32 v167, v0
	s_add_u32 s85, s20, 0x100
	s_addc_u32 s89, s21, 0
	v_lshl_add_u64 v[178:179], s[80:81], 0, v[166:167]
	v_lshl_add_u64 v[180:181], s[80:81], 0, v[162:163]
	s_mov_b32 s92, -2
	s_mov_b64 s[90:91], 0
	s_waitcnt vmcnt(0)
	v_add_u32_e32 v2, s23, v197
	v_add_u32_e32 v14, s66, v197
	s_add_u32 s8, s90, 0x100
	ds_read_b128 v[18:21], v2
	ds_read_b128 v[22:25], v2 offset:1024
	ds_read_b128 v[26:29], v2 offset:2048
	ds_read_b128 v[30:33], v2 offset:3072
	ds_read_b128 v[2:5], v14
	ds_read_b128 v[6:9], v14 offset:1024
	ds_read_b128 v[10:13], v14 offset:2048
	ds_read_b128 v[14:17], v14 offset:3072
	s_addc_u32 s9, s91, 0
	s_add_u32 s62, s85, s90
	s_addc_u32 s63, s89, s91
	s_cmpk_eq_i32 s90, 0x300
	s_cselect_b64 vcc, -1, 0
	s_and_b64 s[20:21], vcc, exec
	v_cndmask_b32_e32 v188, v164, v200, vcc
	v_cndmask_b32_e32 v186, v168, v201, vcc
	v_cndmask_b32_e32 v163, v162, v202, vcc
	v_cndmask_b32_e32 v165, v166, v203, vcc
	s_cselect_b32 s21, s87, s63
	s_cselect_b32 s20, s86, s62
	s_cselect_b32 s62, 0, s8
	v_lshl_add_u64 v[182:183], v[180:181], 0, s[90:91]
	s_add_i32 m0, s68, 0xc000
	ds_read_b128 v[218:221], v199
	ds_read_b128 v[222:225], v199 offset:1024
	ds_read_b128 v[226:229], v199 offset:2048
	ds_read_b128 v[230:233], v199 offset:3072
	ds_read_b128 v[234:237], v199 offset:4096
	ds_read_b128 v[238:241], v199 offset:5120
	ds_read_b128 v[242:245], v199 offset:6144
	ds_read_b128 v[246:249], v199 offset:7168
	global_load_lds_dwordx4 v[182:183], off
	v_lshl_add_u64 v[182:183], v[178:179], 0, s[90:91]
	s_add_i32 m0, s68, 0xe000
	s_nop 0
	global_load_lds_dwordx4 v[182:183], off
	s_waitcnt vmcnt(8)
	s_waitcnt lgkmcnt(0)
	s_barrier
	s_setprio 1
	s_waitcnt lgkmcnt(0)
	v_mfma_f32_16x16x128_f8f6f4 v[158:161], v[18:25], v[218:225], 0
	v_mfma_f32_16x16x128_f8f6f4 v[154:157], v[26:33], v[218:225], 0
	v_mfma_f32_16x16x128_f8f6f4 v[142:145], v[18:25], v[226:233], 0
	v_mfma_f32_16x16x128_f8f6f4 v[138:141], v[26:33], v[226:233], 0
	v_mfma_f32_16x16x128_f8f6f4 v[126:129], v[18:25], v[234:241], 0
	v_mfma_f32_16x16x128_f8f6f4 v[122:125], v[26:33], v[234:241], 0
	v_mfma_f32_16x16x128_f8f6f4 v[110:113], v[18:25], v[242:249], 0
	v_mfma_f32_16x16x128_f8f6f4 v[106:109], v[26:33], v[242:249], 0
	s_setprio 0
	s_setprio 1
	v_mfma_f32_16x16x128_f8f6f4 v[150:153], v[2:9], v[218:225], 0
	v_mfma_f32_16x16x128_f8f6f4 v[146:149], v[10:17], v[218:225], 0
	v_mfma_f32_16x16x128_f8f6f4 v[134:137], v[2:9], v[226:233], 0
	v_mfma_f32_16x16x128_f8f6f4 v[130:133], v[10:17], v[226:233], 0
	v_mfma_f32_16x16x128_f8f6f4 v[118:121], v[2:9], v[234:241], 0
	v_mfma_f32_16x16x128_f8f6f4 v[114:117], v[10:17], v[234:241], 0
	v_mfma_f32_16x16x128_f8f6f4 v[102:105], v[2:9], v[242:249], 0
	v_mfma_f32_16x16x128_f8f6f4 v[98:101], v[10:17], v[242:249], 0
	s_setprio 0
	s_barrier
	s_mov_b32 m0, s59
	v_lshl_add_u64 v[182:183], s[20:21], 0, v[170:171]
	s_add_u32 s90, s20, 0x20000
	ds_read_b128 v[218:221], v199 offset:16384
	ds_read_b128 v[222:225], v199 offset:17408
	ds_read_b128 v[226:229], v199 offset:18432
	ds_read_b128 v[230:233], v199 offset:19456
	ds_read_b128 v[234:237], v199 offset:20480
	ds_read_b128 v[238:241], v199 offset:21504
	ds_read_b128 v[242:245], v199 offset:22528
	ds_read_b128 v[246:249], v199 offset:23552
	global_load_lds_dwordx4 v[182:183], off
	v_lshl_add_u64 v[184:185], s[20:21], 0, v[172:173]
	s_mov_b32 m0, s65
	s_addc_u32 s91, s21, 0
	global_load_lds_dwordx4 v[184:185], off
	v_lshl_add_u64 v[204:205], s[90:91], 0, v[170:171]
	s_mov_b32 m0, s67
	v_mov_b32_e32 v189, v0
	global_load_lds_dwordx4 v[204:205], off
	v_lshl_add_u64 v[204:205], s[90:91], 0, v[172:173]
	s_mov_b32 m0, s10
	s_add_u32 s90, s12, s62
	global_load_lds_dwordx4 v[204:205], off
	s_addc_u32 s91, s13, 0
	s_mov_b32 m0, s68
	v_mov_b32_e32 v187, v0
	global_load_lds_dwordx4 v188, s[90:91]
	s_mov_b32 m0, s71
	v_lshl_add_u64 v[188:189], s[90:91], 0, v[188:189]
	global_load_lds_dwordx4 v186, s[90:91]
	s_waitcnt vmcnt(8)
	s_waitcnt lgkmcnt(0)
	v_lshl_add_u64 v[186:187], s[90:91], 0, v[186:187]
	s_barrier
	s_setprio 1
	s_waitcnt lgkmcnt(0)
	v_mfma_f32_16x16x128_f8f6f4 v[94:97], v[18:25], v[218:225], 0
	v_mfma_f32_16x16x128_f8f6f4 v[90:93], v[26:33], v[218:225], 0
	v_mfma_f32_16x16x128_f8f6f4 v[78:81], v[18:25], v[226:233], 0
	v_mfma_f32_16x16x128_f8f6f4 v[74:77], v[26:33], v[226:233], 0
	v_mfma_f32_16x16x128_f8f6f4 v[54:57], v[18:25], v[234:241], 0
	v_mfma_f32_16x16x128_f8f6f4 v[50:53], v[26:33], v[234:241], 0
	v_mfma_f32_16x16x128_f8f6f4 v[38:41], v[18:25], v[242:249], 0
	v_mfma_f32_16x16x128_f8f6f4 v[34:37], v[26:33], v[242:249], 0
	s_setprio 0
	s_setprio 1
	v_mfma_f32_16x16x128_f8f6f4 v[86:89], v[2:9], v[218:225], 0
	v_mfma_f32_16x16x128_f8f6f4 v[82:85], v[10:17], v[218:225], 0
	v_mfma_f32_16x16x128_f8f6f4 v[70:73], v[2:9], v[226:233], 0
	v_mfma_f32_16x16x128_f8f6f4 v[66:69], v[10:17], v[226:233], 0
	v_mfma_f32_16x16x128_f8f6f4 v[62:65], v[2:9], v[234:241], 0
	v_mfma_f32_16x16x128_f8f6f4 v[58:61], v[10:17], v[234:241], 0
	v_mfma_f32_16x16x128_f8f6f4 v[46:49], v[2:9], v[242:249], 0
	v_mfma_f32_16x16x128_f8f6f4 v[42:45], v[10:17], v[242:249], 0
	s_setprio 0
	s_barrier
	v_add_u32_e32 v14, s3, v197
	v_add_u32_e32 v30, s52, v197
	ds_read_b128 v[2:5], v14
	ds_read_b128 v[6:9], v14 offset:1024
	ds_read_b128 v[10:13], v14 offset:2048
	ds_read_b128 v[14:17], v14 offset:3072
	ds_read_b128 v[18:21], v30
	ds_read_b128 v[22:25], v30 offset:1024
	ds_read_b128 v[26:29], v30 offset:2048
	ds_read_b128 v[30:33], v30 offset:3072
	s_mov_b32 m0, s72
	ds_read_b128 v[218:221], v199 offset:32768
	ds_read_b128 v[222:225], v199 offset:33792
	ds_read_b128 v[226:229], v199 offset:34816
	ds_read_b128 v[230:233], v199 offset:35840
	ds_read_b128 v[234:237], v199 offset:36864
	ds_read_b128 v[238:241], v199 offset:37888
	ds_read_b128 v[242:245], v199 offset:38912
	ds_read_b128 v[246:249], v199 offset:39936
	global_load_lds_dwordx4 v163, s[90:91]
	s_mov_b32 m0, s73
	s_nop 0
	global_load_lds_dwordx4 v165, s[90:91]
	s_waitcnt vmcnt(8)
	s_waitcnt lgkmcnt(0)
	s_barrier
	s_setprio 1
	s_waitcnt lgkmcnt(0)
	v_mfma_f32_16x16x128_f8f6f4 v[158:161], v[2:9], v[218:225], v[158:161]
	v_mfma_f32_16x16x128_f8f6f4 v[154:157], v[10:17], v[218:225], v[154:157]
	v_mfma_f32_16x16x128_f8f6f4 v[142:145], v[2:9], v[226:233], v[142:145]
	v_mfma_f32_16x16x128_f8f6f4 v[138:141], v[10:17], v[226:233], v[138:141]
	v_mfma_f32_16x16x128_f8f6f4 v[126:129], v[2:9], v[234:241], v[126:129]
	v_mfma_f32_16x16x128_f8f6f4 v[122:125], v[10:17], v[234:241], v[122:125]
	v_mfma_f32_16x16x128_f8f6f4 v[110:113], v[2:9], v[242:249], v[110:113]
	v_mfma_f32_16x16x128_f8f6f4 v[106:109], v[10:17], v[242:249], v[106:109]
	s_setprio 0
	s_setprio 1
	v_mfma_f32_16x16x128_f8f6f4 v[150:153], v[18:25], v[218:225], v[150:153]
	v_mfma_f32_16x16x128_f8f6f4 v[146:149], v[26:33], v[218:225], v[146:149]
	v_mfma_f32_16x16x128_f8f6f4 v[134:137], v[18:25], v[226:233], v[134:137]
	v_mfma_f32_16x16x128_f8f6f4 v[130:133], v[26:33], v[226:233], v[130:133]
	v_mfma_f32_16x16x128_f8f6f4 v[118:121], v[18:25], v[234:241], v[118:121]
	v_mfma_f32_16x16x128_f8f6f4 v[114:117], v[26:33], v[234:241], v[114:117]
	v_mfma_f32_16x16x128_f8f6f4 v[102:105], v[18:25], v[242:249], v[102:105]
	v_mfma_f32_16x16x128_f8f6f4 v[98:101], v[26:33], v[242:249], v[98:101]
	s_setprio 0
	s_barrier
	s_mov_b32 m0, s64
	v_lshl_add_u64 v[182:183], v[182:183], 0, s[38:39]
	s_add_u32 s20, s20, 0x20080
	ds_read_b128 v[218:221], v199 offset:49152
	ds_read_b128 v[222:225], v199 offset:50176
	ds_read_b128 v[226:229], v199 offset:51200
	ds_read_b128 v[230:233], v199 offset:52224
	ds_read_b128 v[234:237], v199 offset:53248
	ds_read_b128 v[238:241], v199 offset:54272
	ds_read_b128 v[242:245], v199 offset:55296
	ds_read_b128 v[246:249], v199 offset:56320
	global_load_lds_dwordx4 v[182:183], off
	v_lshl_add_u64 v[182:183], v[184:185], 0, s[38:39]
	s_mov_b32 m0, s2
	s_addc_u32 s21, s21, 0
	global_load_lds_dwordx4 v[182:183], off
	v_lshl_add_u64 v[182:183], s[20:21], 0, v[170:171]
	s_mov_b32 m0, s69
	s_nop 0
	global_load_lds_dwordx4 v[182:183], off
	v_lshl_add_u64 v[182:183], s[20:21], 0, v[172:173]
	s_mov_b32 m0, s51
	s_nop 0
	global_load_lds_dwordx4 v[182:183], off
	v_lshl_add_u64 v[182:183], v[188:189], 0, s[38:39]
	s_mov_b32 m0, s45
	s_nop 0
	global_load_lds_dwordx4 v[182:183], off
	v_lshl_add_u64 v[182:183], v[186:187], 0, s[38:39]
	s_mov_b32 m0, s27
	s_nop 0
	global_load_lds_dwordx4 v[182:183], off
	s_waitcnt vmcnt(8)
	s_waitcnt lgkmcnt(0)
	s_barrier
	s_setprio 1
	s_waitcnt lgkmcnt(0)
	v_mfma_f32_16x16x128_f8f6f4 v[94:97], v[2:9], v[218:225], v[94:97]
	v_mfma_f32_16x16x128_f8f6f4 v[90:93], v[10:17], v[218:225], v[90:93]
	v_mfma_f32_16x16x128_f8f6f4 v[78:81], v[2:9], v[226:233], v[78:81]
	v_mfma_f32_16x16x128_f8f6f4 v[74:77], v[10:17], v[226:233], v[74:77]
	v_mfma_f32_16x16x128_f8f6f4 v[54:57], v[2:9], v[234:241], v[54:57]
	v_mfma_f32_16x16x128_f8f6f4 v[50:53], v[10:17], v[234:241], v[50:53]
	v_mfma_f32_16x16x128_f8f6f4 v[38:41], v[2:9], v[242:249], v[38:41]
	v_mfma_f32_16x16x128_f8f6f4 v[34:37], v[10:17], v[242:249], v[34:37]
	s_setprio 0
	s_setprio 1
	v_mfma_f32_16x16x128_f8f6f4 v[86:89], v[18:25], v[218:225], v[86:89]
	v_mfma_f32_16x16x128_f8f6f4 v[82:85], v[26:33], v[218:225], v[82:85]
	v_mfma_f32_16x16x128_f8f6f4 v[70:73], v[18:25], v[226:233], v[70:73]
	v_mfma_f32_16x16x128_f8f6f4 v[66:69], v[26:33], v[226:233], v[66:69]
	v_mfma_f32_16x16x128_f8f6f4 v[62:65], v[18:25], v[234:241], v[62:65]
	v_mfma_f32_16x16x128_f8f6f4 v[58:61], v[26:33], v[234:241], v[58:61]
	v_mfma_f32_16x16x128_f8f6f4 v[46:49], v[18:25], v[242:249], v[46:49]
	v_mfma_f32_16x16x128_f8f6f4 v[42:45], v[26:33], v[242:249], v[42:45]
	s_setprio 0
	s_barrier
	s_add_i32 s92, s92, 2
	s_cmp_gt_u32 s92, 5
	s_mov_b64 s[90:91], s[8:9]
.LBB0_243:
	v_add_u32_e32 v2, s23, v197
	v_add_u32_e32 v14, s66, v197
	s_add_u32 s8, s90, 0x100
	ds_read_b128 v[18:21], v2
	ds_read_b128 v[22:25], v2 offset:1024
	ds_read_b128 v[26:29], v2 offset:2048
	ds_read_b128 v[30:33], v2 offset:3072
	ds_read_b128 v[2:5], v14
	ds_read_b128 v[6:9], v14 offset:1024
	ds_read_b128 v[10:13], v14 offset:2048
	ds_read_b128 v[14:17], v14 offset:3072
	s_addc_u32 s9, s91, 0
	s_add_u32 s62, s85, s90
	s_addc_u32 s63, s89, s91
	s_cmpk_eq_i32 s90, 0x300
	s_cselect_b64 vcc, -1, 0
	s_and_b64 s[20:21], vcc, exec
	v_cndmask_b32_e32 v188, v164, v200, vcc
	v_cndmask_b32_e32 v186, v168, v201, vcc
	v_cndmask_b32_e32 v163, v162, v202, vcc
	v_cndmask_b32_e32 v165, v166, v203, vcc
	s_cselect_b32 s21, s87, s63
	s_cselect_b32 s20, s86, s62
	s_cselect_b32 s62, 0, s8
	v_lshl_add_u64 v[182:183], v[180:181], 0, s[90:91]
	s_add_i32 m0, s68, 0xc000
	ds_read_b128 v[218:221], v199
	ds_read_b128 v[222:225], v199 offset:1024
	ds_read_b128 v[226:229], v199 offset:2048
	ds_read_b128 v[230:233], v199 offset:3072
	ds_read_b128 v[234:237], v199 offset:4096
	ds_read_b128 v[238:241], v199 offset:5120
	ds_read_b128 v[242:245], v199 offset:6144
	ds_read_b128 v[246:249], v199 offset:7168
	global_load_lds_dwordx4 v[182:183], off
	v_lshl_add_u64 v[182:183], v[178:179], 0, s[90:91]
	s_add_i32 m0, s68, 0xe000
	s_nop 0
	global_load_lds_dwordx4 v[182:183], off
	s_waitcnt vmcnt(8)
	s_waitcnt lgkmcnt(0)
	s_barrier
	s_setprio 1
	s_waitcnt lgkmcnt(0)
	v_mfma_f32_16x16x128_f8f6f4 v[158:161], v[18:25], v[218:225], v[158:161]
	v_mfma_f32_16x16x128_f8f6f4 v[154:157], v[26:33], v[218:225], v[154:157]
	v_mfma_f32_16x16x128_f8f6f4 v[142:145], v[18:25], v[226:233], v[142:145]
	v_mfma_f32_16x16x128_f8f6f4 v[138:141], v[26:33], v[226:233], v[138:141]
	v_mfma_f32_16x16x128_f8f6f4 v[126:129], v[18:25], v[234:241], v[126:129]
	v_mfma_f32_16x16x128_f8f6f4 v[122:125], v[26:33], v[234:241], v[122:125]
	v_mfma_f32_16x16x128_f8f6f4 v[110:113], v[18:25], v[242:249], v[110:113]
	v_mfma_f32_16x16x128_f8f6f4 v[106:109], v[26:33], v[242:249], v[106:109]
	s_setprio 0
	s_setprio 1
	v_mfma_f32_16x16x128_f8f6f4 v[150:153], v[2:9], v[218:225], v[150:153]
	v_mfma_f32_16x16x128_f8f6f4 v[146:149], v[10:17], v[218:225], v[146:149]
	v_mfma_f32_16x16x128_f8f6f4 v[134:137], v[2:9], v[226:233], v[134:137]
	v_mfma_f32_16x16x128_f8f6f4 v[130:133], v[10:17], v[226:233], v[130:133]
	v_mfma_f32_16x16x128_f8f6f4 v[118:121], v[2:9], v[234:241], v[118:121]
	v_mfma_f32_16x16x128_f8f6f4 v[114:117], v[10:17], v[234:241], v[114:117]
	v_mfma_f32_16x16x128_f8f6f4 v[102:105], v[2:9], v[242:249], v[102:105]
	v_mfma_f32_16x16x128_f8f6f4 v[98:101], v[10:17], v[242:249], v[98:101]
	s_setprio 0
	s_barrier
	s_mov_b32 m0, s59
	v_lshl_add_u64 v[182:183], s[20:21], 0, v[170:171]
	s_add_u32 s90, s20, 0x20000
	ds_read_b128 v[218:221], v199 offset:16384
	ds_read_b128 v[222:225], v199 offset:17408
	ds_read_b128 v[226:229], v199 offset:18432
	ds_read_b128 v[230:233], v199 offset:19456
	ds_read_b128 v[234:237], v199 offset:20480
	ds_read_b128 v[238:241], v199 offset:21504
	ds_read_b128 v[242:245], v199 offset:22528
	ds_read_b128 v[246:249], v199 offset:23552
	global_load_lds_dwordx4 v[182:183], off
	v_lshl_add_u64 v[184:185], s[20:21], 0, v[172:173]
	s_mov_b32 m0, s65
	s_addc_u32 s91, s21, 0
	global_load_lds_dwordx4 v[184:185], off
	v_lshl_add_u64 v[204:205], s[90:91], 0, v[170:171]
	s_mov_b32 m0, s67
	v_mov_b32_e32 v189, v0
	global_load_lds_dwordx4 v[204:205], off
	v_lshl_add_u64 v[204:205], s[90:91], 0, v[172:173]
	s_mov_b32 m0, s10
	s_add_u32 s90, s12, s62
	global_load_lds_dwordx4 v[204:205], off
	s_addc_u32 s91, s13, 0
	s_mov_b32 m0, s68
	v_mov_b32_e32 v187, v0
	global_load_lds_dwordx4 v188, s[90:91]
	s_mov_b32 m0, s71
	v_lshl_add_u64 v[188:189], s[90:91], 0, v[188:189]
	global_load_lds_dwordx4 v186, s[90:91]
	s_waitcnt vmcnt(8)
	s_waitcnt lgkmcnt(0)
	v_lshl_add_u64 v[186:187], s[90:91], 0, v[186:187]
	s_barrier
	s_setprio 1
	s_waitcnt lgkmcnt(0)
	v_mfma_f32_16x16x128_f8f6f4 v[94:97], v[18:25], v[218:225], v[94:97]
	v_mfma_f32_16x16x128_f8f6f4 v[90:93], v[26:33], v[218:225], v[90:93]
	v_mfma_f32_16x16x128_f8f6f4 v[78:81], v[18:25], v[226:233], v[78:81]
	v_mfma_f32_16x16x128_f8f6f4 v[74:77], v[26:33], v[226:233], v[74:77]
	v_mfma_f32_16x16x128_f8f6f4 v[54:57], v[18:25], v[234:241], v[54:57]
	v_mfma_f32_16x16x128_f8f6f4 v[50:53], v[26:33], v[234:241], v[50:53]
	v_mfma_f32_16x16x128_f8f6f4 v[38:41], v[18:25], v[242:249], v[38:41]
	v_mfma_f32_16x16x128_f8f6f4 v[34:37], v[26:33], v[242:249], v[34:37]
	s_setprio 0
	s_setprio 1
	v_mfma_f32_16x16x128_f8f6f4 v[86:89], v[2:9], v[218:225], v[86:89]
	v_mfma_f32_16x16x128_f8f6f4 v[82:85], v[10:17], v[218:225], v[82:85]
	v_mfma_f32_16x16x128_f8f6f4 v[70:73], v[2:9], v[226:233], v[70:73]
	v_mfma_f32_16x16x128_f8f6f4 v[66:69], v[10:17], v[226:233], v[66:69]
	v_mfma_f32_16x16x128_f8f6f4 v[62:65], v[2:9], v[234:241], v[62:65]
	v_mfma_f32_16x16x128_f8f6f4 v[58:61], v[10:17], v[234:241], v[58:61]
	v_mfma_f32_16x16x128_f8f6f4 v[46:49], v[2:9], v[242:249], v[46:49]
	v_mfma_f32_16x16x128_f8f6f4 v[42:45], v[10:17], v[242:249], v[42:45]
	s_setprio 0
	s_barrier
	v_add_u32_e32 v14, s3, v197
	v_add_u32_e32 v30, s52, v197
	ds_read_b128 v[2:5], v14
	ds_read_b128 v[6:9], v14 offset:1024
	ds_read_b128 v[10:13], v14 offset:2048
	ds_read_b128 v[14:17], v14 offset:3072
	ds_read_b128 v[18:21], v30
	ds_read_b128 v[22:25], v30 offset:1024
	ds_read_b128 v[26:29], v30 offset:2048
	ds_read_b128 v[30:33], v30 offset:3072
	s_mov_b32 m0, s72
	ds_read_b128 v[218:221], v199 offset:32768
	ds_read_b128 v[222:225], v199 offset:33792
	ds_read_b128 v[226:229], v199 offset:34816
	ds_read_b128 v[230:233], v199 offset:35840
	ds_read_b128 v[234:237], v199 offset:36864
	ds_read_b128 v[238:241], v199 offset:37888
	ds_read_b128 v[242:245], v199 offset:38912
	ds_read_b128 v[246:249], v199 offset:39936
	global_load_lds_dwordx4 v163, s[90:91]
	s_mov_b32 m0, s73
	s_nop 0
	global_load_lds_dwordx4 v165, s[90:91]
	s_waitcnt vmcnt(8)
	s_waitcnt lgkmcnt(0)
	s_barrier
	s_setprio 1
	s_waitcnt lgkmcnt(0)
	v_mfma_f32_16x16x128_f8f6f4 v[158:161], v[2:9], v[218:225], v[158:161]
	v_mfma_f32_16x16x128_f8f6f4 v[154:157], v[10:17], v[218:225], v[154:157]
	v_mfma_f32_16x16x128_f8f6f4 v[142:145], v[2:9], v[226:233], v[142:145]
	v_mfma_f32_16x16x128_f8f6f4 v[138:141], v[10:17], v[226:233], v[138:141]
	v_mfma_f32_16x16x128_f8f6f4 v[126:129], v[2:9], v[234:241], v[126:129]
	v_mfma_f32_16x16x128_f8f6f4 v[122:125], v[10:17], v[234:241], v[122:125]
	v_mfma_f32_16x16x128_f8f6f4 v[110:113], v[2:9], v[242:249], v[110:113]
	v_mfma_f32_16x16x128_f8f6f4 v[106:109], v[10:17], v[242:249], v[106:109]
	s_setprio 0
	s_setprio 1
	v_mfma_f32_16x16x128_f8f6f4 v[150:153], v[18:25], v[218:225], v[150:153]
	v_mfma_f32_16x16x128_f8f6f4 v[146:149], v[26:33], v[218:225], v[146:149]
	v_mfma_f32_16x16x128_f8f6f4 v[134:137], v[18:25], v[226:233], v[134:137]
	v_mfma_f32_16x16x128_f8f6f4 v[130:133], v[26:33], v[226:233], v[130:133]
	v_mfma_f32_16x16x128_f8f6f4 v[118:121], v[18:25], v[234:241], v[118:121]
	v_mfma_f32_16x16x128_f8f6f4 v[114:117], v[26:33], v[234:241], v[114:117]
	v_mfma_f32_16x16x128_f8f6f4 v[102:105], v[18:25], v[242:249], v[102:105]
	v_mfma_f32_16x16x128_f8f6f4 v[98:101], v[26:33], v[242:249], v[98:101]
	s_setprio 0
	s_barrier
	s_mov_b32 m0, s64
	v_lshl_add_u64 v[182:183], v[182:183], 0, s[38:39]
	s_add_u32 s20, s20, 0x20080
	ds_read_b128 v[218:221], v199 offset:49152
	ds_read_b128 v[222:225], v199 offset:50176
	ds_read_b128 v[226:229], v199 offset:51200
	ds_read_b128 v[230:233], v199 offset:52224
	ds_read_b128 v[234:237], v199 offset:53248
	ds_read_b128 v[238:241], v199 offset:54272
	ds_read_b128 v[242:245], v199 offset:55296
	ds_read_b128 v[246:249], v199 offset:56320
	global_load_lds_dwordx4 v[182:183], off
	v_lshl_add_u64 v[182:183], v[184:185], 0, s[38:39]
	s_mov_b32 m0, s2
	s_addc_u32 s21, s21, 0
	global_load_lds_dwordx4 v[182:183], off
	v_lshl_add_u64 v[182:183], s[20:21], 0, v[170:171]
	s_mov_b32 m0, s69
	s_nop 0
	global_load_lds_dwordx4 v[182:183], off
	v_lshl_add_u64 v[182:183], s[20:21], 0, v[172:173]
	s_mov_b32 m0, s51
	s_nop 0
	global_load_lds_dwordx4 v[182:183], off
	v_lshl_add_u64 v[182:183], v[188:189], 0, s[38:39]
	s_mov_b32 m0, s45
	s_nop 0
	global_load_lds_dwordx4 v[182:183], off
	v_lshl_add_u64 v[182:183], v[186:187], 0, s[38:39]
	s_mov_b32 m0, s27
	s_nop 0
	global_load_lds_dwordx4 v[182:183], off
	s_waitcnt vmcnt(8)
	s_waitcnt lgkmcnt(0)
	s_barrier
	s_setprio 1
	s_waitcnt lgkmcnt(0)
	v_mfma_f32_16x16x128_f8f6f4 v[94:97], v[2:9], v[218:225], v[94:97]
	v_mfma_f32_16x16x128_f8f6f4 v[90:93], v[10:17], v[218:225], v[90:93]
	v_mfma_f32_16x16x128_f8f6f4 v[78:81], v[2:9], v[226:233], v[78:81]
	v_mfma_f32_16x16x128_f8f6f4 v[74:77], v[10:17], v[226:233], v[74:77]
	v_mfma_f32_16x16x128_f8f6f4 v[54:57], v[2:9], v[234:241], v[54:57]
	v_mfma_f32_16x16x128_f8f6f4 v[50:53], v[10:17], v[234:241], v[50:53]
	v_mfma_f32_16x16x128_f8f6f4 v[38:41], v[2:9], v[242:249], v[38:41]
	v_mfma_f32_16x16x128_f8f6f4 v[34:37], v[10:17], v[242:249], v[34:37]
	s_setprio 0
	s_setprio 1
	v_mfma_f32_16x16x128_f8f6f4 v[86:89], v[18:25], v[218:225], v[86:89]
	v_mfma_f32_16x16x128_f8f6f4 v[82:85], v[26:33], v[218:225], v[82:85]
	v_mfma_f32_16x16x128_f8f6f4 v[70:73], v[18:25], v[226:233], v[70:73]
	v_mfma_f32_16x16x128_f8f6f4 v[66:69], v[26:33], v[226:233], v[66:69]
	v_mfma_f32_16x16x128_f8f6f4 v[62:65], v[18:25], v[234:241], v[62:65]
	v_mfma_f32_16x16x128_f8f6f4 v[58:61], v[26:33], v[234:241], v[58:61]
	v_mfma_f32_16x16x128_f8f6f4 v[46:49], v[18:25], v[242:249], v[46:49]
	v_mfma_f32_16x16x128_f8f6f4 v[42:45], v[26:33], v[242:249], v[42:45]
	s_setprio 0
	s_barrier
	s_add_i32 s92, s92, 2
	s_cmp_gt_u32 s92, 5
	s_mov_b64 s[90:91], s[8:9]
	s_cbranch_scc0 .LBB0_243
	s_and_b64 vcc, exec, s[82:83]
	s_cbranch_vccz .LBB0_246
	s_barrier

.LBB0_430:
	s_waitcnt lgkmcnt(0)
	v_mfma_scale_f32_32x32x64_f8f6f4 v[144:159], v[184:191], v[192:199], v[96:111], v207, v218 op_sel_hi:[0,0,0]
	ds_read_b128 v[2:5], v221
	ds_read_b128 v[184:187], v221 offset:2048
	ds_read_b128 v[6:9], v222
	ds_read_b128 v[168:171], v221 offset:4096
	ds_read_b128 v[188:191], v222 offset:2048
	ds_read_b128 v[172:175], v222 offset:4096
	v_cvt_pknorm_u16_f32 v1, v112, v113
	v_cvt_pknorm_u16_f32 v10, v114, v115
	v_perm_b32 v160, v10, v1, s55
	v_cvt_pknorm_u16_f32 v1, v116, v117
	v_cvt_pknorm_u16_f32 v10, v118, v119
	v_perm_b32 v161, v10, v1, s55
	v_cvt_pknorm_u16_f32 v1, v120, v121
	v_cvt_pknorm_u16_f32 v10, v122, v123
	v_perm_b32 v162, v10, v1, s55
	v_cvt_pknorm_u16_f32 v1, v124, v125
	v_cvt_pknorm_u16_f32 v10, v126, v127
	v_perm_b32 v163, v10, v1, s55
	s_waitcnt lgkmcnt(6)
	v_mfma_scale_f32_32x32x64_f8f6f4 v[112:127], v[176:183], v[192:199], v[96:111], v207, v218 op_sel_hi:[0,0,0]
	s_add_u32 s52, s4, s84
	s_addc_u32 s54, s5, s85
	s_add_u32 s14, s52, 0xa000
	s_addc_u32 s15, s54, 0
	v_cvt_pknorm_u16_f32 v1, v128, v129
	v_cvt_pknorm_u16_f32 v10, v130, v131
	s_add_u32 s56, s6, s84
	v_perm_b32 v164, v10, v1, s55
	v_cvt_pknorm_u16_f32 v1, v132, v133
	v_cvt_pknorm_u16_f32 v10, v134, v135
	s_addc_u32 s61, s7, s85
	v_perm_b32 v165, v10, v1, s55
	v_cvt_pknorm_u16_f32 v1, v136, v137
	v_cvt_pknorm_u16_f32 v10, v138, v139
	s_add_u32 s20, s56, 0xa000
	v_perm_b32 v166, v10, v1, s55
	v_cvt_pknorm_u16_f32 v1, v140, v141
	v_cvt_pknorm_u16_f32 v10, v142, v143
	s_addc_u32 s21, s61, 0
	v_perm_b32 v167, v10, v1, s55
	s_mov_b32 m0, s45
	v_lshl_add_u64 v[10:11], s[14:15], 0, v[200:201]
	global_load_lds_dwordx4 v[10:11], off
	v_lshl_add_u64 v[10:11], s[20:21], 0, v[202:203]
	s_add_i32 m0, s23, 0xc800
	s_nop 0
	global_load_lds_dwordx4 v[10:11], off
	s_waitcnt lgkmcnt(0)
	v_mfma_f32_32x32x64_f8f6f4 v[64:79], v[2:9], v[160:167], v[64:79]
	ds_read_b128 v[136:139], v221 offset:6144
	ds_read_b128 v[140:143], v222 offset:6144
	v_mfma_f32_32x32x64_f8f6f4 v[48:63], v[184:191], v[160:167], v[48:63]
	ds_read_b128 v[128:131], v219 offset:16384
	ds_read_b128 v[2:5], v219 offset:20480
	ds_read_b128 v[132:135], v220 offset:16384
	ds_read_b128 v[6:9], v220 offset:20480
	v_mov_b32_e32 v1, v144
	v_max3_f32 v1, v1, v144, v145
	v_max3_f32 v1, v1, v146, v147
	v_max3_f32 v1, v1, v148, v149
	v_max3_f32 v1, v1, v150, v151
	v_max3_f32 v1, v1, v152, v153
	v_max3_f32 v1, v1, v154, v155
	v_max3_f32 v1, v1, v156, v157
	v_max3_f32 v1, v1, v158, v159
	v_mfma_f32_32x32x64_f8f6f4 v[32:47], v[168:175], v[160:167], v[32:47]
	v_max3_f32 v1, v1, v112, v113
	v_max3_f32 v1, v1, v114, v115
	v_max3_f32 v1, v1, v116, v117
	v_max3_f32 v1, v1, v118, v119
	v_max3_f32 v1, v1, v120, v121
	v_max3_f32 v1, v1, v122, v123
	v_max3_f32 v1, v1, v124, v125
	v_max3_f32 v1, v1, v126, v127
	v_cmp_ge_f32_e32 vcc, s53, v1
	s_cmp_eq_u64 vcc, exec
	s_waitcnt lgkmcnt(0)
	v_mfma_f32_32x32x64_f8f6f4 v[16:31], v[136:143], v[160:167], v[16:31]
	v_mfma_f32_16x16x128_f8f6f4 v[248:251], v[240:247], v[160:167], v[248:251]
	s_cbranch_scc0 .LBB0_438
.LBB0_431:
	s_waitcnt vmcnt(4)
	s_waitcnt lgkmcnt(0)
	s_barrier
	v_mfma_scale_f32_32x32x64_f8f6f4 v[160:175], v[128:135], v[192:199], v[96:111], v207, v218 op_sel_hi:[0,0,0]
	ds_read_b128 v[224:227], v221 offset:10240
	ds_read_b128 v[232:235], v221 offset:12288
	ds_read_b128 v[228:231], v222 offset:10240
	ds_read_b128 v[136:139], v221 offset:14336
	ds_read_b128 v[236:239], v222 offset:12288
	ds_read_b128 v[140:143], v222 offset:14336
	v_cvt_pknorm_u16_f32 v1, v144, v145
	v_cvt_pknorm_u16_f32 v10, v146, v147
	v_perm_b32 v128, v10, v1, s55
	v_cvt_pknorm_u16_f32 v1, v148, v149
	v_cvt_pknorm_u16_f32 v10, v150, v151
	v_perm_b32 v129, v10, v1, s55
	v_cvt_pknorm_u16_f32 v1, v152, v153
	v_cvt_pknorm_u16_f32 v10, v154, v155
	v_perm_b32 v130, v10, v1, s55
	v_cvt_pknorm_u16_f32 v1, v156, v157
	v_cvt_pknorm_u16_f32 v10, v158, v159
	v_perm_b32 v131, v10, v1, s55
	v_mfma_scale_f32_32x32x64_f8f6f4 v[176:191], v[2:9], v[192:199], v[96:111], v207, v218 op_sel_hi:[0,0,0]
	v_cvt_pknorm_u16_f32 v1, v112, v113
	v_cvt_pknorm_u16_f32 v2, v114, v115
	s_add_u32 s14, s52, 0xc000
	v_perm_b32 v132, v2, v1, s55
	v_cvt_pknorm_u16_f32 v1, v116, v117
	v_cvt_pknorm_u16_f32 v2, v118, v119
	s_addc_u32 s15, s54, 0
	v_perm_b32 v133, v2, v1, s55
	v_cvt_pknorm_u16_f32 v1, v120, v121
	v_cvt_pknorm_u16_f32 v2, v122, v123
	s_add_u32 s20, s56, 0xc000
	v_perm_b32 v134, v2, v1, s55
	v_cvt_pknorm_u16_f32 v1, v124, v125
	v_cvt_pknorm_u16_f32 v2, v126, v127
	s_addc_u32 s21, s61, 0
	v_perm_b32 v135, v2, v1, s55
	s_mov_b32 m0, s59
	v_lshl_add_u64 v[2:3], s[14:15], 0, v[200:201]
	global_load_lds_dwordx4 v[2:3], off
	v_lshl_add_u64 v[2:3], s[20:21], 0, v[202:203]
	s_mov_b32 m0, s23
	s_nop 0
	global_load_lds_dwordx4 v[2:3], off
	s_waitcnt lgkmcnt(0)
	v_mfma_f32_32x32x64_f8f6f4 v[64:79], v[224:231], v[128:135], v[64:79]
	ds_read_b128 v[120:123], v221 offset:16384
	ds_read_b128 v[124:127], v222 offset:16384
	v_mfma_f32_32x32x64_f8f6f4 v[48:63], v[232:239], v[128:135], v[48:63]
	ds_read_b128 v[112:115], v219 offset:24576
	ds_read_b128 v[2:5], v219 offset:28672
	ds_read_b128 v[116:119], v220 offset:24576
	ds_read_b128 v[6:9], v220 offset:28672
	v_mov_b32_e32 v1, v160
	v_max3_f32 v1, v1, v160, v161
	v_max3_f32 v1, v1, v162, v163
	v_max3_f32 v1, v1, v164, v165
	v_max3_f32 v1, v1, v166, v167
	v_max3_f32 v1, v1, v168, v169
	v_max3_f32 v1, v1, v170, v171
	v_max3_f32 v1, v1, v172, v173
	v_max3_f32 v1, v1, v174, v175
	v_mfma_f32_32x32x64_f8f6f4 v[32:47], v[136:143], v[128:135], v[32:47]
	v_max3_f32 v1, v1, v176, v177
	v_max3_f32 v1, v1, v178, v179
	v_max3_f32 v1, v1, v180, v181
	v_max3_f32 v1, v1, v182, v183
	v_max3_f32 v1, v1, v184, v185
	v_max3_f32 v1, v1, v186, v187
	v_max3_f32 v1, v1, v188, v189
	v_max3_f32 v1, v1, v190, v191
	v_cmp_ge_f32_e32 vcc, s53, v1
	s_cmp_eq_u64 vcc, exec
	s_waitcnt lgkmcnt(0)
	v_mfma_f32_32x32x64_f8f6f4 v[16:31], v[120:127], v[128:135], v[16:31]
	v_mfma_f32_16x16x128_f8f6f4 v[248:251], v[240:247], v[128:135], v[248:251]
	s_cbranch_scc0 .LBB0_441
.LBB0_432:
	s_waitcnt vmcnt(4)
	s_waitcnt lgkmcnt(0)
	s_barrier
	v_mfma_scale_f32_32x32x64_f8f6f4 v[128:143], v[112:119], v[192:199], v[96:111], v207, v218 op_sel_hi:[0,0,0]
	ds_read_b128 v[224:227], v221 offset:20480
	ds_read_b128 v[232:235], v221 offset:22528
	ds_read_b128 v[228:231], v222 offset:20480
	ds_read_b128 v[120:123], v221 offset:24576
	ds_read_b128 v[236:239], v222 offset:22528
	ds_read_b128 v[124:127], v222 offset:24576
	v_cvt_pknorm_u16_f32 v1, v160, v161
	v_cvt_pknorm_u16_f32 v10, v162, v163
	v_perm_b32 v112, v10, v1, s55
	v_cvt_pknorm_u16_f32 v1, v164, v165
	v_cvt_pknorm_u16_f32 v10, v166, v167
	v_perm_b32 v113, v10, v1, s55
	v_cvt_pknorm_u16_f32 v1, v168, v169
	v_cvt_pknorm_u16_f32 v10, v170, v171
	v_perm_b32 v114, v10, v1, s55
	v_cvt_pknorm_u16_f32 v1, v172, v173
	v_cvt_pknorm_u16_f32 v10, v174, v175
	v_perm_b32 v115, v10, v1, s55
	v_mfma_scale_f32_32x32x64_f8f6f4 v[144:159], v[2:9], v[192:199], v[96:111], v207, v218 op_sel_hi:[0,0,0]
	v_cvt_pknorm_u16_f32 v1, v176, v177
	v_cvt_pknorm_u16_f32 v2, v178, v179
	s_add_u32 s14, s52, 0xe000
	v_perm_b32 v116, v2, v1, s55
	v_cvt_pknorm_u16_f32 v1, v180, v181
	v_cvt_pknorm_u16_f32 v2, v182, v183
	s_addc_u32 s15, s54, 0
	v_perm_b32 v117, v2, v1, s55
	v_cvt_pknorm_u16_f32 v1, v184, v185
	v_cvt_pknorm_u16_f32 v2, v186, v187
	s_add_u32 s20, s56, 0xe000
	v_perm_b32 v118, v2, v1, s55
	v_cvt_pknorm_u16_f32 v1, v188, v189
	v_cvt_pknorm_u16_f32 v2, v190, v191
	s_addc_u32 s21, s61, 0
	v_perm_b32 v119, v2, v1, s55
	s_mov_b32 m0, s48
	v_lshl_add_u64 v[2:3], s[14:15], 0, v[200:201]
	global_load_lds_dwordx4 v[2:3], off
	v_lshl_add_u64 v[2:3], s[20:21], 0, v[202:203]
	s_mov_b32 m0, s2
	s_nop 0
	global_load_lds_dwordx4 v[2:3], off
	s_waitcnt lgkmcnt(0)
	v_mfma_f32_32x32x64_f8f6f4 v[64:79], v[224:231], v[112:119], v[64:79]
	ds_read_b128 v[168:171], v221 offset:26624
	ds_read_b128 v[172:175], v222 offset:26624
	v_mfma_f32_32x32x64_f8f6f4 v[48:63], v[232:239], v[112:119], v[48:63]
	ds_read_b128 v[160:163], v219 offset:32768
	ds_read_b128 v[2:5], v219 offset:36864
	ds_read_b128 v[164:167], v220 offset:32768
	ds_read_b128 v[6:9], v220 offset:36864
	v_mov_b32_e32 v1, v128
	v_max3_f32 v1, v1, v128, v129
	v_max3_f32 v1, v1, v130, v131
	v_max3_f32 v1, v1, v132, v133
	v_max3_f32 v1, v1, v134, v135
	v_max3_f32 v1, v1, v136, v137
	v_max3_f32 v1, v1, v138, v139
	v_max3_f32 v1, v1, v140, v141
	v_max3_f32 v1, v1, v142, v143
	v_mfma_f32_32x32x64_f8f6f4 v[32:47], v[120:127], v[112:119], v[32:47]
	v_max3_f32 v1, v1, v144, v145
	v_max3_f32 v1, v1, v146, v147
	v_max3_f32 v1, v1, v148, v149
	v_max3_f32 v1, v1, v150, v151
	v_max3_f32 v1, v1, v152, v153
	v_max3_f32 v1, v1, v154, v155
	v_max3_f32 v1, v1, v156, v157
	v_max3_f32 v1, v1, v158, v159
	v_cmp_ge_f32_e32 vcc, s53, v1
	s_cmp_eq_u64 vcc, exec
	s_waitcnt lgkmcnt(0)
	v_mfma_f32_32x32x64_f8f6f4 v[16:31], v[168:175], v[112:119], v[16:31]
	v_mfma_f32_16x16x128_f8f6f4 v[248:251], v[240:247], v[112:119], v[248:251]
	s_cbranch_scc0 .LBB0_444
.LBB0_433:
	s_waitcnt vmcnt(4)
	s_waitcnt lgkmcnt(0)
	s_barrier
	v_mfma_scale_f32_32x32x64_f8f6f4 v[112:127], v[160:167], v[192:199], v[96:111], v207, v218 op_sel_hi:[0,0,0]
	ds_read_b128 v[184:187], v221 offset:30720
	ds_read_b128 v[228:231], v222 offset:32768
	ds_read_b128 v[224:227], v221 offset:32768
	ds_read_b128 v[176:179], v221 offset:34816
	ds_read_b128 v[188:191], v222 offset:30720
	ds_read_b128 v[180:183], v222 offset:34816
	v_cvt_pknorm_u16_f32 v1, v128, v129
	v_cvt_pknorm_u16_f32 v10, v130, v131
	v_perm_b32 v128, v10, v1, s55
	v_cvt_pknorm_u16_f32 v1, v132, v133
	v_cvt_pknorm_u16_f32 v10, v134, v135
	v_perm_b32 v129, v10, v1, s55
	v_cvt_pknorm_u16_f32 v1, v136, v137
	v_cvt_pknorm_u16_f32 v10, v138, v139
	v_perm_b32 v130, v10, v1, s55
	v_cvt_pknorm_u16_f32 v1, v140, v141
	v_cvt_pknorm_u16_f32 v10, v142, v143
	v_perm_b32 v131, v10, v1, s55
	v_mfma_scale_f32_32x32x64_f8f6f4 v[160:175], v[2:9], v[192:199], v[96:111], v207, v218 op_sel_hi:[0,0,0]
	s_add_i32 s14, s33, -2
	s_min_u32 s14, s14, s17
	s_lshl_b32 s20, s14, 13
	v_cvt_pknorm_u16_f32 v1, v144, v145
	v_cvt_pknorm_u16_f32 v2, v146, v147
	s_add_u32 s14, s4, s20
	v_perm_b32 v132, v2, v1, s55
	v_cvt_pknorm_u16_f32 v1, v148, v149
	v_cvt_pknorm_u16_f32 v2, v150, v151
	s_addc_u32 s15, s5, 0
	v_perm_b32 v133, v2, v1, s55
	v_cvt_pknorm_u16_f32 v1, v152, v153
	v_cvt_pknorm_u16_f32 v2, v154, v155
	s_add_u32 s20, s6, s20
	v_perm_b32 v134, v2, v1, s55
	v_cvt_pknorm_u16_f32 v1, v156, v157
	v_cvt_pknorm_u16_f32 v2, v158, v159
	s_addc_u32 s21, s7, 0
	v_perm_b32 v135, v2, v1, s55
	s_mov_b32 m0, s49
	v_lshl_add_u64 v[2:3], s[14:15], 0, v[200:201]
	global_load_lds_dwordx4 v[2:3], off
	v_lshl_add_u64 v[2:3], s[20:21], 0, v[202:203]
	s_mov_b32 m0, s3
	s_nop 0
	global_load_lds_dwordx4 v[2:3], off
	s_waitcnt lgkmcnt(0)
	v_mfma_f32_32x32x64_f8f6f4 v[64:79], v[184:191], v[128:135], v[64:79]
	ds_read_b128 v[136:139], v221 offset:36864
	ds_read_b128 v[140:143], v222 offset:36864
	v_mfma_f32_32x32x64_f8f6f4 v[48:63], v[224:231], v[128:135], v[48:63]
	ds_read_b128 v[144:147], v219 offset:40960
	ds_read_b128 v[2:5], v219 offset:45056
	ds_read_b128 v[148:151], v220 offset:40960
	ds_read_b128 v[6:9], v220 offset:45056
	v_mov_b32_e32 v1, v112
	v_max3_f32 v1, v1, v112, v113
	v_max3_f32 v1, v1, v114, v115
	v_max3_f32 v1, v1, v116, v117
	v_max3_f32 v1, v1, v118, v119
	v_max3_f32 v1, v1, v120, v121
	v_max3_f32 v1, v1, v122, v123
	v_max3_f32 v1, v1, v124, v125
	v_max3_f32 v1, v1, v126, v127
	v_mfma_f32_32x32x64_f8f6f4 v[32:47], v[176:183], v[128:135], v[32:47]
	v_max3_f32 v1, v1, v160, v161
	v_max3_f32 v1, v1, v162, v163
	v_max3_f32 v1, v1, v164, v165
	v_max3_f32 v1, v1, v166, v167
	v_max3_f32 v1, v1, v168, v169
	v_max3_f32 v1, v1, v170, v171
	v_max3_f32 v1, v1, v172, v173
	v_max3_f32 v1, v1, v174, v175
	v_cmp_ge_f32_e32 vcc, s53, v1
	s_cmp_eq_u64 vcc, exec
	s_waitcnt lgkmcnt(0)
	v_mfma_f32_32x32x64_f8f6f4 v[16:31], v[136:143], v[128:135], v[16:31]
	v_mfma_f32_16x16x128_f8f6f4 v[248:251], v[240:247], v[128:135], v[248:251]
	s_cbranch_scc0 .LBB0_447
.LBB0_434:
	s_waitcnt vmcnt(4)
	s_waitcnt lgkmcnt(0)
	s_barrier
	v_mfma_scale_f32_32x32x64_f8f6f4 v[128:143], v[144:151], v[192:199], v[96:111], v207, v218 op_sel_hi:[0,0,0]
	ds_read_b128 v[184:187], v221 offset:40960
	ds_read_b128 v[224:227], v221 offset:43008
	ds_read_b128 v[188:191], v222 offset:40960
	ds_read_b128 v[176:179], v221 offset:45056
	ds_read_b128 v[228:231], v222 offset:43008
	ds_read_b128 v[180:183], v222 offset:45056
	v_cvt_pknorm_u16_f32 v1, v112, v113
	v_cvt_pknorm_u16_f32 v10, v114, v115
	v_perm_b32 v112, v10, v1, s55
	v_cvt_pknorm_u16_f32 v1, v116, v117
	v_cvt_pknorm_u16_f32 v10, v118, v119
	v_perm_b32 v113, v10, v1, s55
	v_cvt_pknorm_u16_f32 v1, v120, v121
	v_cvt_pknorm_u16_f32 v10, v122, v123
	v_perm_b32 v114, v10, v1, s55
	v_cvt_pknorm_u16_f32 v1, v124, v125
	v_cvt_pknorm_u16_f32 v10, v126, v127
	v_perm_b32 v115, v10, v1, s55
	v_mfma_scale_f32_32x32x64_f8f6f4 v[144:159], v[2:9], v[192:199], v[96:111], v207, v218 op_sel_hi:[0,0,0]
	s_add_i32 s14, s33, -1
	s_min_u32 s14, s14, s17
	s_lshl_b32 s20, s14, 13
	v_cvt_pknorm_u16_f32 v1, v160, v161
	v_cvt_pknorm_u16_f32 v2, v162, v163
	s_add_u32 s14, s4, s20
	v_perm_b32 v116, v2, v1, s55
	v_cvt_pknorm_u16_f32 v1, v164, v165
	v_cvt_pknorm_u16_f32 v2, v166, v167
	s_addc_u32 s15, s5, 0
	v_perm_b32 v117, v2, v1, s55
	v_cvt_pknorm_u16_f32 v1, v168, v169
	v_cvt_pknorm_u16_f32 v2, v170, v171
	s_add_u32 s20, s6, s20
	v_perm_b32 v118, v2, v1, s55
	v_cvt_pknorm_u16_f32 v1, v172, v173
	v_cvt_pknorm_u16_f32 v2, v174, v175
	s_addc_u32 s21, s7, 0
	v_perm_b32 v119, v2, v1, s55
	s_mov_b32 m0, s50
	v_lshl_add_u64 v[2:3], s[14:15], 0, v[200:201]
	global_load_lds_dwordx4 v[2:3], off
	v_lshl_add_u64 v[2:3], s[20:21], 0, v[202:203]
	s_mov_b32 m0, s27
	s_nop 0
	global_load_lds_dwordx4 v[2:3], off
	s_waitcnt lgkmcnt(0)
	v_mfma_f32_32x32x64_f8f6f4 v[64:79], v[184:191], v[112:119], v[64:79]
	ds_read_b128 v[120:123], v221 offset:47104
	ds_read_b128 v[124:127], v222 offset:47104
	v_mfma_f32_32x32x64_f8f6f4 v[48:63], v[224:231], v[112:119], v[48:63]
	ds_read_b128 v[160:163], v219
	ds_read_b128 v[2:5], v219 offset:4096
	ds_read_b128 v[164:167], v220
	ds_read_b128 v[6:9], v220 offset:4096
	v_mov_b32_e32 v1, v128
	v_max3_f32 v1, v1, v128, v129
	v_max3_f32 v1, v1, v130, v131
	v_max3_f32 v1, v1, v132, v133
	v_max3_f32 v1, v1, v134, v135
	v_max3_f32 v1, v1, v136, v137
	v_max3_f32 v1, v1, v138, v139
	v_max3_f32 v1, v1, v140, v141
	v_max3_f32 v1, v1, v142, v143
	v_mfma_f32_32x32x64_f8f6f4 v[32:47], v[176:183], v[112:119], v[32:47]
	v_max3_f32 v1, v1, v144, v145
	v_max3_f32 v1, v1, v146, v147
	v_max3_f32 v1, v1, v148, v149
	v_max3_f32 v1, v1, v150, v151
	v_max3_f32 v1, v1, v152, v153
	v_max3_f32 v1, v1, v154, v155
	v_max3_f32 v1, v1, v156, v157
	v_max3_f32 v1, v1, v158, v159
	v_cmp_ge_f32_e32 vcc, s53, v1
	s_cmp_eq_u64 vcc, exec
	s_waitcnt lgkmcnt(0)
	v_mfma_f32_32x32x64_f8f6f4 v[16:31], v[120:127], v[112:119], v[16:31]
	v_mfma_f32_16x16x128_f8f6f4 v[248:251], v[240:247], v[112:119], v[248:251]
	s_cbranch_scc0 .LBB0_450
.LBB0_435:
	s_waitcnt vmcnt(4)
	s_waitcnt lgkmcnt(0)
	s_barrier
	v_mfma_scale_f32_32x32x64_f8f6f4 v[112:127], v[160:167], v[192:199], v[96:111], v207, v218 op_sel_hi:[0,0,0]
	ds_read_b128 v[176:179], v221 offset:51200
	ds_read_b128 v[184:187], v221 offset:53248
	ds_read_b128 v[180:183], v222 offset:51200
	ds_read_b128 v[168:171], v221 offset:55296
	ds_read_b128 v[188:191], v222 offset:53248
	ds_read_b128 v[172:175], v222 offset:55296
	v_cvt_pknorm_u16_f32 v1, v128, v129
	v_cvt_pknorm_u16_f32 v10, v130, v131
	v_perm_b32 v160, v10, v1, s55
	v_cvt_pknorm_u16_f32 v1, v132, v133
	v_cvt_pknorm_u16_f32 v10, v134, v135
	v_perm_b32 v161, v10, v1, s55
	v_cvt_pknorm_u16_f32 v1, v136, v137
	v_cvt_pknorm_u16_f32 v10, v138, v139
	v_perm_b32 v162, v10, v1, s55
	v_cvt_pknorm_u16_f32 v1, v140, v141
	v_cvt_pknorm_u16_f32 v10, v142, v143
	v_perm_b32 v163, v10, v1, s55
	v_mfma_scale_f32_32x32x64_f8f6f4 v[128:143], v[2:9], v[192:199], v[96:111], v207, v218 op_sel_hi:[0,0,0]
	s_min_u32 s14, s33, s17
	s_lshl_b32 s20, s14, 13
	v_cvt_pknorm_u16_f32 v1, v144, v145
	v_cvt_pknorm_u16_f32 v2, v146, v147
	s_add_u32 s14, s4, s20
	v_perm_b32 v164, v2, v1, s55
	v_cvt_pknorm_u16_f32 v1, v148, v149
	v_cvt_pknorm_u16_f32 v2, v150, v151
	s_addc_u32 s15, s5, 0
	v_perm_b32 v165, v2, v1, s55
	v_cvt_pknorm_u16_f32 v1, v152, v153
	v_cvt_pknorm_u16_f32 v2, v154, v155
	s_add_u32 s20, s6, s20
	v_perm_b32 v166, v2, v1, s55
	v_cvt_pknorm_u16_f32 v1, v156, v157
	v_cvt_pknorm_u16_f32 v2, v158, v159
	s_addc_u32 s21, s7, 0
	v_perm_b32 v167, v2, v1, s55
	s_mov_b32 m0, s51
	v_lshl_add_u64 v[2:3], s[14:15], 0, v[200:201]
	global_load_lds_dwordx4 v[2:3], off
	v_lshl_add_u64 v[2:3], s[20:21], 0, v[202:203]
	s_mov_b32 m0, s26
	s_nop 0
	global_load_lds_dwordx4 v[2:3], off
	s_waitcnt lgkmcnt(0)
	v_mfma_f32_32x32x64_f8f6f4 v[64:79], v[176:183], v[160:167], v[64:79]
	ds_read_b128 v[2:5], v221 offset:57344
	ds_read_b128 v[6:9], v222 offset:57344
	v_mfma_f32_32x32x64_f8f6f4 v[48:63], v[184:191], v[160:167], v[48:63]
	ds_read_b128 v[184:187], v219 offset:8192
	ds_read_b128 v[176:179], v219 offset:12288
	ds_read_b128 v[188:191], v220 offset:8192
	ds_read_b128 v[180:183], v220 offset:12288
	v_mov_b32_e32 v1, v112
	v_max3_f32 v1, v1, v112, v113
	v_max3_f32 v1, v1, v114, v115
	v_max3_f32 v1, v1, v116, v117
	v_max3_f32 v1, v1, v118, v119
	v_max3_f32 v1, v1, v120, v121
	v_max3_f32 v1, v1, v122, v123
	v_max3_f32 v1, v1, v124, v125
	v_max3_f32 v1, v1, v126, v127
	v_mfma_f32_32x32x64_f8f6f4 v[32:47], v[168:175], v[160:167], v[32:47]
	v_max3_f32 v1, v1, v128, v129
	v_max3_f32 v1, v1, v130, v131
	v_max3_f32 v1, v1, v132, v133
	v_max3_f32 v1, v1, v134, v135
	v_max3_f32 v1, v1, v136, v137
	v_max3_f32 v1, v1, v138, v139
	v_max3_f32 v1, v1, v140, v141
	v_max3_f32 v1, v1, v142, v143
	v_cmp_ge_f32_e32 vcc, s53, v1
	s_cmp_eq_u64 vcc, exec
	s_waitcnt lgkmcnt(0)
	v_mfma_f32_32x32x64_f8f6f4 v[16:31], v[2:9], v[160:167], v[16:31]
	v_mfma_f32_16x16x128_f8f6f4 v[248:251], v[240:247], v[160:167], v[248:251]
	s_cbranch_scc0 .LBB0_453

.LBB0_465:
	s_mul_hi_u32 s14, s2, 0xaaaaaaab
	s_lshr_b32 s14, s14, 2
	s_mul_i32 s14, s14, 0xc000
	v_subrev_u32_e32 v10, s14, v220
	v_subrev_u32_e32 v212, s14, v219
	s_mul_hi_u32 s14, s23, 0xaaaaaaab
	s_lshr_b32 s14, s14, 2
	s_mul_i32 s15, s14, 0xffff1000
	s_add_i32 s59, s21, s15
	s_mul_hi_u32 s15, s48, 0xaaaaaaab
	s_mul_i32 s14, s14, 0xffff4000
	s_lshr_b32 s54, s15, 2
	s_add_i32 s14, s26, s14
	s_mul_i32 s56, s54, 0xffff1000
	s_add_i32 s61, s49, -1
	s_waitcnt lgkmcnt(0)
	v_mfma_scale_f32_32x32x64_f8f6f4 v[144:159], v[184:191], v[192:199], v[96:111], v207, v218 op_sel_hi:[0,0,0]
	s_add_i32 s15, s45, s51
	s_add_i32 s62, s15, s56
	v_add_u32_e32 v214, s62, v12
	v_add_u32_e32 v215, s62, v11
	ds_read_b128 v[2:5], v214
	ds_read_b128 v[184:187], v214 offset:2048
	ds_read_b128 v[6:9], v215
	ds_read_b128 v[222:225], v214 offset:4096
	ds_read_b128 v[188:191], v215 offset:2048
	ds_read_b128 v[226:229], v215 offset:4096
	v_cvt_pknorm_u16_f32 v14, v112, v113
	v_cvt_pknorm_u16_f32 v15, v114, v115
	v_perm_b32 v112, v15, v14, s55
	v_cvt_pknorm_u16_f32 v14, v116, v117
	v_cvt_pknorm_u16_f32 v15, v118, v119
	v_perm_b32 v113, v15, v14, s55
	v_cvt_pknorm_u16_f32 v14, v120, v121
	v_cvt_pknorm_u16_f32 v15, v122, v123
	v_perm_b32 v114, v15, v14, s55
	v_cvt_pknorm_u16_f32 v14, v124, v125
	v_cvt_pknorm_u16_f32 v15, v126, v127
	v_perm_b32 v115, v15, v14, s55
	v_mfma_scale_f32_32x32x64_f8f6f4 v[160:175], v[176:183], v[192:199], v[96:111], v207, v218 op_sel_hi:[0,0,0]
	s_min_u32 s61, s61, s17
	s_lshl_b32 s61, s61, 13
	v_cvt_pknorm_u16_f32 v14, v128, v129
	v_cvt_pknorm_u16_f32 v15, v130, v131
	s_add_u32 s62, s4, s61
	v_perm_b32 v116, v15, v14, s55
	v_cvt_pknorm_u16_f32 v14, v132, v133
	v_cvt_pknorm_u16_f32 v15, v134, v135
	s_addc_u32 s63, s5, 0
	v_perm_b32 v117, v15, v14, s55
	v_cvt_pknorm_u16_f32 v14, v136, v137
	v_cvt_pknorm_u16_f32 v15, v138, v139
	s_add_u32 s64, s6, s61
	v_perm_b32 v118, v15, v14, s55
	v_cvt_pknorm_u16_f32 v14, v140, v141
	v_cvt_pknorm_u16_f32 v15, v142, v143
	s_addc_u32 s65, s7, 0
	s_add_i32 s61, s14, s90
	s_add_i32 s14, s3, s52
	s_add_i32 s59, s59, s90
	v_perm_b32 v119, v15, v14, s55
	s_add_i32 m0, s14, s61
	v_lshl_add_u64 v[14:15], s[62:63], 0, v[200:201]
	s_add_i32 s59, s59, s20
	global_load_lds_dwordx4 v[14:15], off
	v_lshl_add_u64 v[14:15], s[64:65], 0, v[202:203]
	s_add_i32 m0, s59, s51
	s_nop 0
	global_load_lds_dwordx4 v[14:15], off
	s_nop 4
	s_waitcnt lgkmcnt(0)
	v_mfma_f32_32x32x64_f8f6f4 v[64:79], v[2:9], v[112:119], v[64:79]
	ds_read_b128 v[120:123], v214 offset:6144
	ds_read_b128 v[124:127], v215 offset:6144
	v_add_u32_e32 v2, s14, v212
	v_add_u32_e32 v6, s14, v10
	v_mfma_f32_32x32x64_f8f6f4 v[48:63], v[184:191], v[112:119], v[48:63]
	ds_read_b128 v[136:139], v214 offset:8192
	ds_read_b128 v[140:143], v215 offset:8192
	ds_read_b128 v[128:131], v2 offset:8192
	ds_read_b128 v[2:5], v2 offset:12288
	ds_read_b128 v[132:135], v6 offset:8192
	ds_read_b128 v[6:9], v6 offset:12288
	v_mov_b32_e32 v14, v144
	v_max3_f32 v14, v14, v144, v145
	v_max3_f32 v14, v14, v146, v147
	v_max3_f32 v14, v14, v148, v149
	v_max3_f32 v14, v14, v150, v151
	v_max3_f32 v14, v14, v152, v153
	v_max3_f32 v14, v14, v154, v155
	v_max3_f32 v14, v14, v156, v157
	v_max3_f32 v14, v14, v158, v159
	v_mfma_f32_32x32x64_f8f6f4 v[32:47], v[222:229], v[112:119], v[32:47]
	s_nop 0
	v_max3_f32 v14, v14, v160, v161
	v_max3_f32 v14, v14, v162, v163
	v_max3_f32 v14, v14, v164, v165
	v_max3_f32 v14, v14, v166, v167
	v_max3_f32 v14, v14, v168, v169
	v_max3_f32 v14, v14, v170, v171
	v_max3_f32 v14, v14, v172, v173
	v_max3_f32 v14, v14, v174, v175
	s_nop 0
	v_cmp_ge_f32_e32 vcc, s53, v14
	s_cmp_eq_u64 vcc, exec
	s_waitcnt lgkmcnt(0)
	v_mfma_f32_32x32x64_f8f6f4 v[16:31], v[120:127], v[112:119], v[16:31]
	v_mfma_f32_32x32x64_f8f6f4 v[80:95], v[136:143], v[112:119], v[80:95]
	s_cbranch_scc0 .LBB0_469
.LBB0_466:
	s_mul_hi_u32 s59, s27, 0xaaaaaaab
	s_lshr_b32 s59, s59, 2
	s_mul_i32 s59, s59, 0xc000
	s_waitcnt vmcnt(4)
	s_waitcnt lgkmcnt(0)
	s_barrier
	v_subrev_u32_e32 v10, s59, v220
	v_subrev_u32_e32 v14, s59, v219
	s_mul_hi_u32 s59, s33, 0xaaaaaaab
	s_lshr_b32 s59, s59, 2
	s_mul_i32 s54, s54, 0xffff4000
	s_mul_i32 s59, s59, 0xffff1000
	s_add_i32 s56, s22, s56
	s_add_i32 s54, s50, s54
	v_mfma_scale_f32_32x32x64_f8f6f4 v[112:127], v[128:135], v[192:199], v[96:111], v207, v218 op_sel_hi:[0,0,0]
	s_add_i32 s15, s15, s59
	v_add_u32_e32 v15, s15, v1
	v_add_u32_e32 v212, s15, v13
	ds_read_b128 v[176:179], v15
	ds_read_b128 v[184:187], v15 offset:2048
	ds_read_b128 v[180:183], v212
	ds_read_b128 v[222:225], v15 offset:4096
	ds_read_b128 v[188:191], v212 offset:2048
	ds_read_b128 v[226:229], v212 offset:4096
	v_cvt_pknorm_u16_f32 v128, v144, v145
	v_cvt_pknorm_u16_f32 v129, v146, v147
	v_perm_b32 v144, v129, v128, s55
	v_cvt_pknorm_u16_f32 v128, v148, v149
	v_cvt_pknorm_u16_f32 v129, v150, v151
	v_perm_b32 v145, v129, v128, s55
	v_cvt_pknorm_u16_f32 v128, v152, v153
	v_cvt_pknorm_u16_f32 v129, v154, v155
	v_perm_b32 v146, v129, v128, s55
	v_cvt_pknorm_u16_f32 v128, v156, v157
	v_cvt_pknorm_u16_f32 v129, v158, v159
	v_perm_b32 v147, v129, v128, s55
	v_mfma_scale_f32_32x32x64_f8f6f4 v[128:143], v[2:9], v[192:199], v[96:111], v207, v218 op_sel_hi:[0,0,0]
	s_min_u32 s15, s49, s17
	s_lshl_b32 s15, s15, 13
	s_add_u32 s62, s4, s15
	s_addc_u32 s63, s5, 0
	v_cvt_pknorm_u16_f32 v2, v160, v161
	v_cvt_pknorm_u16_f32 v3, v162, v163
	s_add_u32 s64, s6, s15
	v_perm_b32 v148, v3, v2, s55
	v_cvt_pknorm_u16_f32 v2, v164, v165
	v_cvt_pknorm_u16_f32 v3, v166, v167
	s_addc_u32 s65, s7, 0
	s_add_i32 s15, s54, s90
	v_perm_b32 v149, v3, v2, s55
	v_cvt_pknorm_u16_f32 v2, v168, v169
	v_cvt_pknorm_u16_f32 v3, v170, v171
	s_add_i32 s15, s15, s3
	v_perm_b32 v150, v3, v2, s55
	v_cvt_pknorm_u16_f32 v2, v172, v173
	v_cvt_pknorm_u16_f32 v3, v174, v175
	s_add_i32 m0, s15, s52
	s_add_i32 s15, s56, s90
	v_perm_b32 v151, v3, v2, s55
	s_add_i32 s15, s15, s20
	v_lshl_add_u64 v[2:3], s[62:63], 0, v[200:201]
	global_load_lds_dwordx4 v[2:3], off
	v_lshl_add_u64 v[2:3], s[64:65], 0, v[202:203]
	s_add_i32 m0, s15, s51
	s_nop 0
	global_load_lds_dwordx4 v[2:3], off
	s_nop 4
	s_waitcnt lgkmcnt(0)
	v_mfma_f32_32x32x64_f8f6f4 v[64:79], v[176:183], v[144:151], v[64:79]
	ds_read_b128 v[152:155], v15 offset:6144
	ds_read_b128 v[156:159], v212 offset:6144
	v_add_u32_e32 v2, s14, v14
	v_mfma_f32_32x32x64_f8f6f4 v[48:63], v[184:191], v[144:151], v[48:63]
	ds_read_b128 v[160:163], v15 offset:8192
	ds_read_b128 v[164:167], v212 offset:8192
	v_add_u32_e32 v3, s14, v10
	ds_read_b128 v[184:187], v2 offset:16384
	ds_read_b128 v[176:179], v2 offset:20480
	ds_read_b128 v[188:191], v3 offset:16384
	ds_read_b128 v[180:183], v3 offset:20480
	v_mov_b32_e32 v3, v112
	v_max3_f32 v3, v3, v112, v113
	v_max3_f32 v3, v3, v114, v115
	v_max3_f32 v3, v3, v116, v117
	v_max3_f32 v3, v3, v118, v119
	v_max3_f32 v3, v3, v120, v121
	v_max3_f32 v3, v3, v122, v123
	v_max3_f32 v3, v3, v124, v125
	v_max3_f32 v3, v3, v126, v127
	v_mfma_f32_32x32x64_f8f6f4 v[32:47], v[222:229], v[144:151], v[32:47]
	s_nop 0
	v_max3_f32 v3, v3, v128, v129
	v_max3_f32 v3, v3, v130, v131
	v_max3_f32 v3, v3, v132, v133
	v_max3_f32 v3, v3, v134, v135
	v_max3_f32 v3, v3, v136, v137
	v_max3_f32 v3, v3, v138, v139
	v_max3_f32 v3, v3, v140, v141
	v_max3_f32 v3, v3, v142, v143
	s_nop 0
	v_cmp_ge_f32_e32 vcc, s53, v3
	s_cmp_eq_u64 vcc, exec
	s_waitcnt lgkmcnt(0)
	v_mfma_f32_32x32x64_f8f6f4 v[16:31], v[152:159], v[144:151], v[16:31]
	v_mfma_f32_32x32x64_f8f6f4 v[80:95], v[160:167], v[144:151], v[80:95]
	s_cbranch_scc0 .LBB0_472

.LBB0_477:
	s_add_i32 s2, s58, -2
	s_mul_hi_u32 s3, s2, 0xaaaaaaab
	s_lshr_b32 s3, s3, 2
	s_mul_i32 s3, s3, 6
	s_sub_i32 s2, s2, s3
	s_waitcnt lgkmcnt(0)
	v_mfma_scale_f32_32x32x64_f8f6f4 v[160:175], v[184:191], v[192:199], v[96:111], v207, v218 op_sel_hi:[0,0,0]
	v_mfma_scale_f32_32x32x64_f8f6f4 v[144:159], v[176:183], v[192:199], v[96:111], v207, v218 op_sel_hi:[0,0,0]
	v_cvt_pknorm_u16_f32 v1, v112, v113
	v_cvt_pknorm_u16_f32 v2, v114, v115
	v_perm_b32 v2, v2, v1, s55
	v_cvt_pknorm_u16_f32 v1, v128, v129
	v_cvt_pknorm_u16_f32 v3, v130, v131
	v_perm_b32 v6, v3, v1, s55
	v_cvt_pknorm_u16_f32 v1, v116, v117
	v_cvt_pknorm_u16_f32 v3, v118, v119
	v_perm_b32 v3, v3, v1, s55
	v_cvt_pknorm_u16_f32 v1, v132, v133
	v_cvt_pknorm_u16_f32 v4, v134, v135
	v_perm_b32 v7, v4, v1, s55
	v_cvt_pknorm_u16_f32 v1, v120, v121
	v_cvt_pknorm_u16_f32 v4, v122, v123
	v_perm_b32 v4, v4, v1, s55
	v_cvt_pknorm_u16_f32 v1, v136, v137
	v_cvt_pknorm_u16_f32 v5, v138, v139
	v_perm_b32 v8, v5, v1, s55
	v_cvt_pknorm_u16_f32 v1, v124, v125
	v_cvt_pknorm_u16_f32 v5, v126, v127
	v_perm_b32 v5, v5, v1, s55
	v_cvt_pknorm_u16_f32 v1, v140, v141
	v_cvt_pknorm_u16_f32 v9, v142, v143
	v_perm_b32 v9, v9, v1, s55
	s_mulk_i32 s2, 0x2800
	s_add_i32 s2, s10, s2
	v_add_u32_e32 v1, s2, v208
	s_nop 4
	v_add_u32_e32 v10, v1, v209
	v_add_u32_e32 v1, v1, v217
	ds_read_b128 v[96:99], v10
	ds_read_b128 v[100:103], v1
	ds_read_b128 v[104:107], v10 offset:2048
	ds_read_b128 v[108:111], v1 offset:2048
	ds_read_b128 v[112:115], v10 offset:4096
	ds_read_b128 v[116:119], v1 offset:4096
	ds_read_b128 v[120:123], v10 offset:6144
	ds_read_b128 v[124:127], v1 offset:6144
	ds_read_b128 v[128:131], v10 offset:8192
	ds_read_b128 v[132:135], v1 offset:8192
	s_waitcnt lgkmcnt(8)
	v_mfma_f32_32x32x64_f8f6f4 v[64:79], v[96:103], v[2:9], v[64:79]
	s_waitcnt lgkmcnt(6)
	v_mfma_f32_32x32x64_f8f6f4 v[48:63], v[104:111], v[2:9], v[48:63]
	s_waitcnt lgkmcnt(4)
	v_mfma_f32_32x32x64_f8f6f4 v[32:47], v[112:119], v[2:9], v[32:47]
	s_waitcnt lgkmcnt(2)
	v_mfma_f32_32x32x64_f8f6f4 v[16:31], v[120:127], v[2:9], v[16:31]
	s_waitcnt lgkmcnt(0)
	v_mfma_f32_32x32x64_f8f6f4 v[80:95], v[128:135], v[2:9], v[80:95]
	v_max_f32_e32 v1, v161, v161
	v_max_f32_e32 v2, v160, v160
	v_max_f32_e32 v1, v2, v1
	v_max3_f32 v1, v1, v162, v163
	v_max3_f32 v1, v1, v164, v165
	v_max3_f32 v1, v1, v166, v167
	v_max3_f32 v1, v1, v168, v169
	v_max3_f32 v1, v1, v170, v171
	v_max3_f32 v1, v1, v172, v173
	v_max3_f32 v1, v1, v174, v175
	v_max3_f32 v1, v1, v144, v145
	v_max3_f32 v1, v1, v146, v147
	v_max3_f32 v1, v1, v148, v149
	v_max3_f32 v1, v1, v150, v151
	v_max3_f32 v1, v1, v152, v153
	v_max3_f32 v1, v1, v154, v155
	v_max3_f32 v1, v1, v156, v157
	v_max3_f32 v1, v1, v158, v159
	v_mov_b32_e32 v2, v1
	s_nop 1
	v_permlane32_swap_b32_e32 v1, v2
	v_max_f32_e32 v2, v2, v2
	v_max_f32_e32 v1, v1, v1
	v_max_f32_e32 v1, v1, v2
	v_cmp_ge_f32_e32 vcc, s53, v1
	v_mov_b32_e32 v2, 1.0
	s_cmp_eq_u64 vcc, exec
	s_cbranch_scc0 .LBB0_485
	v_cmp_gt_f32_e32 vcc, 1.0, v2
	s_cbranch_vccz .LBB0_480

.LBB0_480:
	v_cvt_pknorm_u16_f32 v1, v160, v161
	v_cvt_pknorm_u16_f32 v2, v162, v163
	v_perm_b32 v2, v2, v1, s55
	v_cvt_pknorm_u16_f32 v1, v144, v145
	v_cvt_pknorm_u16_f32 v3, v146, v147
	v_perm_b32 v6, v3, v1, s55
	v_cvt_pknorm_u16_f32 v1, v164, v165
	v_cvt_pknorm_u16_f32 v3, v166, v167
	v_perm_b32 v3, v3, v1, s55
	v_cvt_pknorm_u16_f32 v1, v148, v149
	v_cvt_pknorm_u16_f32 v4, v150, v151
	v_perm_b32 v7, v4, v1, s55
	v_cvt_pknorm_u16_f32 v1, v168, v169
	v_cvt_pknorm_u16_f32 v4, v170, v171
	s_mul_hi_u32 s2, s17, 0xaaaaaaab
	v_perm_b32 v4, v4, v1, s55
	v_cvt_pknorm_u16_f32 v1, v152, v153
	v_cvt_pknorm_u16_f32 v5, v154, v155
	s_lshr_b32 s2, s2, 2
	v_perm_b32 v8, v5, v1, s55
	v_cvt_pknorm_u16_f32 v1, v172, v173
	v_cvt_pknorm_u16_f32 v5, v174, v175
	s_mul_i32 s2, s2, 6
	v_perm_b32 v5, v5, v1, s55
	v_cvt_pknorm_u16_f32 v1, v156, v157
	v_cvt_pknorm_u16_f32 v9, v158, v159
	s_sub_i32 s2, s17, s2
	v_perm_b32 v9, v9, v1, s55
	s_mulk_i32 s2, 0x2800
	s_add_i32 s2, s10, s2
	v_add_u32_e32 v1, s2, v208
	s_nop 4
	v_add_u32_e32 v10, v1, v209
	v_add_u32_e32 v1, v1, v217
	ds_read_b128 v[96:99], v10
	ds_read_b128 v[100:103], v1
	ds_read_b128 v[104:107], v10 offset:2048
	ds_read_b128 v[108:111], v1 offset:2048
	ds_read_b128 v[112:115], v10 offset:4096
	ds_read_b128 v[116:119], v1 offset:4096
	ds_read_b128 v[120:123], v10 offset:6144
	ds_read_b128 v[124:127], v1 offset:6144
	ds_read_b128 v[128:131], v10 offset:8192
	ds_read_b128 v[132:135], v1 offset:8192
	s_mov_b32 s2, s47
	s_waitcnt lgkmcnt(8)
	v_mfma_f32_32x32x64_f8f6f4 v[64:79], v[96:103], v[2:9], v[64:79]
	s_waitcnt lgkmcnt(6)
	v_mfma_f32_32x32x64_f8f6f4 v[48:63], v[104:111], v[2:9], v[48:63]
	s_waitcnt lgkmcnt(4)
	v_mfma_f32_32x32x64_f8f6f4 v[32:47], v[112:119], v[2:9], v[32:47]
	s_waitcnt lgkmcnt(2)
	v_mfma_f32_32x32x64_f8f6f4 v[16:31], v[120:127], v[2:9], v[16:31]
	s_waitcnt lgkmcnt(0)
	v_mfma_f32_32x32x64_f8f6f4 v[80:95], v[128:135], v[2:9], v[80:95]
	s_nop 0
	s_nop 15
	s_nop 15
	v_mbcnt_lo_u32_b32 v2, -1, 0
	v_mbcnt_hi_u32_b32 v2, -1, v2
	s_waitcnt vmcnt(0)
	s_waitcnt vmcnt(0)
	v_lshl_add_u32 v3, s2, 6, v2
	v_and_b32_e32 v252, 15, v2
	v_lshlrev_b32_e32 v252, 2, v252
	ds_bpermute_b32 v253, v252, v248
	ds_bpermute_b32 v254, v252, v249
	v_and_b32_e32 v1, 16, v2
	v_cmp_ne_u32_e32 vcc, 0, v1
	s_waitcnt lgkmcnt(0)
	s_nop 0
	v_cndmask_b32_e32 v253, v253, v254, vcc
	v_add_f32_e32 v80, v80, v253
	v_rcp_f32_e32 v1, v80
	v_lshlrev_b32_e32 v5, 8, v3
	v_and_b32_e32 v5, 0xc000, v5
	v_and_b32_e32 v4, 63, v2
	v_add_u32_e32 v5, s10, v5
	v_and_b32_e32 v6, 0xffffff00, v3
	v_cmp_eq_u32_e32 vcc, s71, v6
	v_lshl_add_u32 v14, v4, 2, v5
	s_barrier
	s_and_saveexec_b64 s[4:5], vcc
	s_cbranch_execz .LBB0_482
	v_mul_f32_e32 v4, v206, v1
	v_mul_f32_e32 v5, v64, v4
	v_mul_f32_e32 v6, v65, v4
	ds_write2st64_b32 v14, v5, v6 offset1:1
	v_mul_f32_e32 v5, v66, v4
	v_mul_f32_e32 v6, v67, v4
	ds_write2st64_b32 v14, v5, v6 offset0:2 offset1:3
	v_mul_f32_e32 v5, v68, v4
	v_mul_f32_e32 v6, v69, v4
	ds_write2st64_b32 v14, v5, v6 offset0:4 offset1:5
	v_mul_f32_e32 v5, v70, v4
	v_mul_f32_e32 v6, v71, v4
	ds_write2st64_b32 v14, v5, v6 offset0:6 offset1:7
	v_mul_f32_e32 v5, v72, v4
	v_mul_f32_e32 v6, v73, v4
	ds_write2st64_b32 v14, v5, v6 offset0:8 offset1:9
	v_mul_f32_e32 v5, v74, v4
	v_mul_f32_e32 v6, v75, v4
	ds_write2st64_b32 v14, v5, v6 offset0:10 offset1:11
	v_mul_f32_e32 v5, v76, v4
	v_mul_f32_e32 v6, v77, v4
	ds_write2st64_b32 v14, v5, v6 offset0:12 offset1:13
	v_mul_f32_e32 v5, v78, v4
	v_mul_f32_e32 v6, v79, v4
	ds_write2st64_b32 v14, v5, v6 offset0:14 offset1:15
	v_mul_f32_e32 v5, v48, v4
	v_mul_f32_e32 v6, v49, v4
	ds_write2st64_b32 v14, v5, v6 offset0:16 offset1:17
	v_mul_f32_e32 v5, v50, v4
	v_mul_f32_e32 v6, v51, v4
	ds_write2st64_b32 v14, v5, v6 offset0:18 offset1:19
	v_mul_f32_e32 v5, v52, v4
	v_mul_f32_e32 v6, v53, v4
	ds_write2st64_b32 v14, v5, v6 offset0:20 offset1:21
	v_mul_f32_e32 v5, v54, v4
	v_mul_f32_e32 v6, v55, v4
	ds_write2st64_b32 v14, v5, v6 offset0:22 offset1:23
	v_mul_f32_e32 v5, v56, v4
	v_mul_f32_e32 v6, v57, v4
	ds_write2st64_b32 v14, v5, v6 offset0:24 offset1:25
	v_mul_f32_e32 v5, v58, v4
	v_mul_f32_e32 v6, v59, v4
	ds_write2st64_b32 v14, v5, v6 offset0:26 offset1:27
	v_mul_f32_e32 v5, v60, v4
	v_mul_f32_e32 v6, v61, v4
	ds_write2st64_b32 v14, v5, v6 offset0:28 offset1:29
	v_mul_f32_e32 v5, v62, v4
	v_mul_f32_e32 v6, v63, v4
	ds_write2st64_b32 v14, v5, v6 offset0:30 offset1:31
	v_mul_f32_e32 v5, v32, v4
	v_mul_f32_e32 v6, v33, v4
	ds_write2st64_b32 v14, v5, v6 offset0:32 offset1:33
	v_mul_f32_e32 v5, v34, v4
	v_mul_f32_e32 v6, v35, v4
	ds_write2st64_b32 v14, v5, v6 offset0:34 offset1:35
	v_mul_f32_e32 v5, v36, v4
	v_mul_f32_e32 v6, v37, v4
	ds_write2st64_b32 v14, v5, v6 offset0:36 offset1:37
	v_mul_f32_e32 v5, v38, v4
	v_mul_f32_e32 v6, v39, v4
	ds_write2st64_b32 v14, v5, v6 offset0:38 offset1:39
	v_mul_f32_e32 v5, v40, v4
	v_mul_f32_e32 v6, v41, v4
	ds_write2st64_b32 v14, v5, v6 offset0:40 offset1:41
	v_mul_f32_e32 v5, v42, v4
	v_mul_f32_e32 v6, v43, v4
	ds_write2st64_b32 v14, v5, v6 offset0:42 offset1:43
	v_mul_f32_e32 v5, v44, v4
	v_mul_f32_e32 v6, v45, v4
	ds_write2st64_b32 v14, v5, v6 offset0:44 offset1:45
	v_mul_f32_e32 v5, v46, v4
	v_mul_f32_e32 v6, v47, v4
	ds_write2st64_b32 v14, v5, v6 offset0:46 offset1:47
	v_mul_f32_e32 v5, v16, v4
	v_mul_f32_e32 v6, v17, v4
	ds_write2st64_b32 v14, v5, v6 offset0:48 offset1:49
	v_mul_f32_e32 v5, v18, v4
	v_mul_f32_e32 v6, v19, v4
	ds_write2st64_b32 v14, v5, v6 offset0:50 offset1:51
	v_mul_f32_e32 v5, v20, v4
	v_mul_f32_e32 v6, v21, v4
	ds_write2st64_b32 v14, v5, v6 offset0:52 offset1:53
	v_mul_f32_e32 v5, v22, v4
	v_mul_f32_e32 v6, v23, v4
	ds_write2st64_b32 v14, v5, v6 offset0:54 offset1:55
	v_mul_f32_e32 v5, v24, v4
	v_mul_f32_e32 v6, v25, v4
	ds_write2st64_b32 v14, v5, v6 offset0:56 offset1:57
	v_mul_f32_e32 v5, v26, v4
	v_mul_f32_e32 v6, v27, v4
	ds_write2st64_b32 v14, v5, v6 offset0:58 offset1:59
	v_mul_f32_e32 v5, v28, v4
	v_mul_f32_e32 v6, v29, v4
	ds_write2st64_b32 v14, v5, v6 offset0:60 offset1:61
	v_mul_f32_e32 v5, v30, v4
	v_mul_f32_e32 v4, v31, v4
	ds_write2st64_b32 v14, v5, v4 offset0:62 offset1:63

.LBB0_619:
	v_add_u32_e32 v2, s6, v188
	v_add_u32_e32 v14, s11, v188
	ds_read_b128 v[18:21], v2
	ds_read_b128 v[22:25], v2 offset:1024
	ds_read_b128 v[26:29], v2 offset:2048
	ds_read_b128 v[30:33], v2 offset:3072
	ds_read_b128 v[2:5], v14
	ds_read_b128 v[6:9], v14 offset:1024
	ds_read_b128 v[10:13], v14 offset:2048
	ds_read_b128 v[14:17], v14 offset:3072
	s_add_u32 s84, s88, 0x100
	s_addc_u32 s85, s89, 0
	s_add_u32 s13, s58, s88
	s_addc_u32 s15, s59, s89
	s_cmp_eq_u32 s14, 4
	s_cselect_b32 s87, s23, s15
	s_cselect_b32 s86, s22, s13
	s_cselect_b32 s13, 0, s84
	v_lshl_add_u64 v[198:199], v[176:177], 0, s[88:89]
	s_add_i32 m0, s19, 0xc000
	ds_read_b128 v[178:181], v189
	ds_read_b128 v[182:185], v189 offset:1024
	ds_read_b128 v[190:193], v189 offset:2048
	ds_read_b128 v[194:197], v189 offset:3072
	ds_read_b128 v[218:221], v189 offset:4096
	ds_read_b128 v[222:225], v189 offset:5120
	ds_read_b128 v[226:229], v189 offset:6144
	ds_read_b128 v[230:233], v189 offset:7168
	global_load_lds_dwordx4 v[198:199], off
	v_lshl_add_u64 v[198:199], v[174:175], 0, s[88:89]
	s_add_i32 m0, s19, 0xe000
	s_nop 0
	global_load_lds_dwordx4 v[198:199], off
	s_waitcnt vmcnt(8)
	s_waitcnt lgkmcnt(0)
	s_barrier
	s_setprio 1
	s_waitcnt lgkmcnt(0)
	v_mfma_f32_16x16x128_f8f6f4 v[158:161], v[18:25], v[178:185], v[158:161]
	v_mfma_f32_16x16x128_f8f6f4 v[154:157], v[26:33], v[178:185], v[154:157]
	v_mfma_f32_16x16x128_f8f6f4 v[142:145], v[18:25], v[190:197], v[142:145]
	v_mfma_f32_16x16x128_f8f6f4 v[138:141], v[26:33], v[190:197], v[138:141]
	v_mfma_f32_16x16x128_f8f6f4 v[126:129], v[18:25], v[218:225], v[126:129]
	v_mfma_f32_16x16x128_f8f6f4 v[122:125], v[26:33], v[218:225], v[122:125]
	v_mfma_f32_16x16x128_f8f6f4 v[110:113], v[18:25], v[226:233], v[110:113]
	v_mfma_f32_16x16x128_f8f6f4 v[106:109], v[26:33], v[226:233], v[106:109]
	s_setprio 0
	s_setprio 1
	v_mfma_f32_16x16x128_f8f6f4 v[150:153], v[2:9], v[178:185], v[150:153]
	v_mfma_f32_16x16x128_f8f6f4 v[146:149], v[10:17], v[178:185], v[146:149]
	v_mfma_f32_16x16x128_f8f6f4 v[134:137], v[2:9], v[190:197], v[134:137]
	v_mfma_f32_16x16x128_f8f6f4 v[130:133], v[10:17], v[190:197], v[130:133]
	v_mfma_f32_16x16x128_f8f6f4 v[118:121], v[2:9], v[218:225], v[118:121]
	v_mfma_f32_16x16x128_f8f6f4 v[114:117], v[10:17], v[218:225], v[114:117]
	v_mfma_f32_16x16x128_f8f6f4 v[102:105], v[2:9], v[226:233], v[102:105]
	v_mfma_f32_16x16x128_f8f6f4 v[98:101], v[10:17], v[226:233], v[98:101]
	s_setprio 0
	s_barrier
	s_mov_b32 m0, s7
	v_lshl_add_u64 v[178:179], s[86:87], 0, v[162:163]
	s_add_u32 s62, s86, 0x20000
	ds_read_b128 v[190:193], v189 offset:16384
	ds_read_b128 v[194:197], v189 offset:17408
	ds_read_b128 v[218:221], v189 offset:18432
	ds_read_b128 v[222:225], v189 offset:19456
	ds_read_b128 v[226:229], v189 offset:20480
	ds_read_b128 v[230:233], v189 offset:21504
	ds_read_b128 v[234:237], v189 offset:22528
	ds_read_b128 v[238:241], v189 offset:23552
	global_load_lds_dwordx4 v[178:179], off
	v_lshl_add_u64 v[180:181], s[86:87], 0, v[164:165]
	s_mov_b32 m0, s10
	s_addc_u32 s63, s87, 0
	global_load_lds_dwordx4 v[180:181], off
	v_lshl_add_u64 v[182:183], s[62:63], 0, v[162:163]
	s_mov_b32 m0, s16
	s_add_u32 s88, s82, s13
	global_load_lds_dwordx4 v[182:183], off
	v_lshl_add_u64 v[182:183], s[62:63], 0, v[164:165]
	s_mov_b32 m0, s18
	s_addc_u32 s89, s83, 0
	global_load_lds_dwordx4 v[182:183], off
	v_lshl_add_u64 v[182:183], s[88:89], 0, v[166:167]
	s_mov_b32 m0, s19
	v_lshl_add_u64 v[184:185], s[88:89], 0, v[170:171]
	global_load_lds_dwordx4 v[182:183], off
	s_mov_b32 m0, s21
	s_nop 0
	global_load_lds_dwordx4 v[184:185], off
	s_waitcnt vmcnt(8)
	s_waitcnt lgkmcnt(0)
	s_barrier
	s_setprio 1
	s_waitcnt lgkmcnt(0)
	v_mfma_f32_16x16x128_f8f6f4 v[94:97], v[18:25], v[190:197], v[94:97]
	v_mfma_f32_16x16x128_f8f6f4 v[90:93], v[26:33], v[190:197], v[90:93]
	v_mfma_f32_16x16x128_f8f6f4 v[78:81], v[18:25], v[218:225], v[78:81]
	v_mfma_f32_16x16x128_f8f6f4 v[74:77], v[26:33], v[218:225], v[74:77]
	v_mfma_f32_16x16x128_f8f6f4 v[58:61], v[18:25], v[226:233], v[58:61]
	v_mfma_f32_16x16x128_f8f6f4 v[42:45], v[26:33], v[226:233], v[42:45]
	v_mfma_f32_16x16x128_f8f6f4 v[38:41], v[18:25], v[234:241], v[38:41]
	v_mfma_f32_16x16x128_f8f6f4 v[34:37], v[26:33], v[234:241], v[34:37]
	s_setprio 0
	s_setprio 1
	v_mfma_f32_16x16x128_f8f6f4 v[86:89], v[2:9], v[190:197], v[86:89]
	v_mfma_f32_16x16x128_f8f6f4 v[82:85], v[10:17], v[190:197], v[82:85]
	v_mfma_f32_16x16x128_f8f6f4 v[62:65], v[2:9], v[218:225], v[62:65]
	v_mfma_f32_16x16x128_f8f6f4 v[46:49], v[10:17], v[218:225], v[46:49]
	v_mfma_f32_16x16x128_f8f6f4 v[70:73], v[2:9], v[226:233], v[70:73]
	v_mfma_f32_16x16x128_f8f6f4 v[66:69], v[10:17], v[226:233], v[66:69]
	v_mfma_f32_16x16x128_f8f6f4 v[54:57], v[2:9], v[234:241], v[54:57]
	v_mfma_f32_16x16x128_f8f6f4 v[50:53], v[10:17], v[234:241], v[50:53]
	s_setprio 0
	s_barrier
	v_add_u32_e32 v14, s45, v188
	v_add_u32_e32 v30, s52, v188
	ds_read_b128 v[2:5], v14
	ds_read_b128 v[6:9], v14 offset:1024
	ds_read_b128 v[10:13], v14 offset:2048
	ds_read_b128 v[14:17], v14 offset:3072
	ds_read_b128 v[18:21], v30
	ds_read_b128 v[22:25], v30 offset:1024
	ds_read_b128 v[26:29], v30 offset:2048
	ds_read_b128 v[30:33], v30 offset:3072
	s_mov_b32 m0, s26
	v_lshl_add_u64 v[198:199], s[88:89], 0, v[168:169]
	ds_read_b128 v[190:193], v189 offset:32768
	ds_read_b128 v[194:197], v189 offset:33792
	ds_read_b128 v[218:221], v189 offset:34816
	ds_read_b128 v[222:225], v189 offset:35840
	ds_read_b128 v[226:229], v189 offset:36864
	ds_read_b128 v[230:233], v189 offset:37888
	ds_read_b128 v[234:237], v189 offset:38912
	ds_read_b128 v[238:241], v189 offset:39936
	global_load_lds_dwordx4 v[198:199], off
	v_lshl_add_u64 v[198:199], s[88:89], 0, v[172:173]
	s_mov_b32 m0, s27
	s_nop 0
	global_load_lds_dwordx4 v[198:199], off
	s_waitcnt vmcnt(8)
	s_waitcnt lgkmcnt(0)
	s_barrier
	s_setprio 1
	s_waitcnt lgkmcnt(0)
	v_mfma_f32_16x16x128_f8f6f4 v[158:161], v[2:9], v[190:197], v[158:161]
	v_mfma_f32_16x16x128_f8f6f4 v[154:157], v[10:17], v[190:197], v[154:157]
	v_mfma_f32_16x16x128_f8f6f4 v[142:145], v[2:9], v[218:225], v[142:145]
	v_mfma_f32_16x16x128_f8f6f4 v[138:141], v[10:17], v[218:225], v[138:141]
	v_mfma_f32_16x16x128_f8f6f4 v[126:129], v[2:9], v[226:233], v[126:129]
	v_mfma_f32_16x16x128_f8f6f4 v[122:125], v[10:17], v[226:233], v[122:125]
	v_mfma_f32_16x16x128_f8f6f4 v[110:113], v[2:9], v[234:241], v[110:113]
	v_mfma_f32_16x16x128_f8f6f4 v[106:109], v[10:17], v[234:241], v[106:109]
	s_setprio 0
	s_setprio 1
	v_mfma_f32_16x16x128_f8f6f4 v[150:153], v[18:25], v[190:197], v[150:153]
	v_mfma_f32_16x16x128_f8f6f4 v[146:149], v[26:33], v[190:197], v[146:149]
	v_mfma_f32_16x16x128_f8f6f4 v[134:137], v[18:25], v[218:225], v[134:137]
	v_mfma_f32_16x16x128_f8f6f4 v[130:133], v[26:33], v[218:225], v[130:133]
	v_mfma_f32_16x16x128_f8f6f4 v[118:121], v[18:25], v[226:233], v[118:121]
	v_mfma_f32_16x16x128_f8f6f4 v[114:117], v[26:33], v[226:233], v[114:117]
	v_mfma_f32_16x16x128_f8f6f4 v[102:105], v[18:25], v[234:241], v[102:105]
	v_mfma_f32_16x16x128_f8f6f4 v[98:101], v[26:33], v[234:241], v[98:101]
	s_setprio 0
	s_barrier
	s_mov_b32 m0, s48
	v_lshl_add_u64 v[178:179], v[178:179], 0, s[38:39]
	s_add_u32 s62, s86, 0x20080
	ds_read_b128 v[190:193], v189 offset:49152
	ds_read_b128 v[194:197], v189 offset:50176
	ds_read_b128 v[218:221], v189 offset:51200
	ds_read_b128 v[222:225], v189 offset:52224
	ds_read_b128 v[226:229], v189 offset:53248
	ds_read_b128 v[230:233], v189 offset:54272
	ds_read_b128 v[234:237], v189 offset:55296
	ds_read_b128 v[238:241], v189 offset:56320
	global_load_lds_dwordx4 v[178:179], off
	v_lshl_add_u64 v[178:179], v[180:181], 0, s[38:39]
	s_mov_b32 m0, s49
	s_addc_u32 s63, s87, 0
	global_load_lds_dwordx4 v[178:179], off
	v_lshl_add_u64 v[178:179], s[62:63], 0, v[162:163]
	s_mov_b32 m0, s54
	s_nop 0
	global_load_lds_dwordx4 v[178:179], off
	v_lshl_add_u64 v[178:179], s[62:63], 0, v[164:165]
	s_mov_b32 m0, s56
	s_nop 0
	global_load_lds_dwordx4 v[178:179], off
	v_lshl_add_u64 v[178:179], v[182:183], 0, s[38:39]
	s_mov_b32 m0, s50
	s_nop 0
	global_load_lds_dwordx4 v[178:179], off
	v_lshl_add_u64 v[178:179], v[184:185], 0, s[38:39]
	s_mov_b32 m0, s51
	s_nop 0
	global_load_lds_dwordx4 v[178:179], off
	s_waitcnt vmcnt(8)
	s_waitcnt lgkmcnt(0)
	s_barrier
	s_setprio 1
	s_waitcnt lgkmcnt(0)
	v_mfma_f32_16x16x128_f8f6f4 v[94:97], v[2:9], v[190:197], v[94:97]
	v_mfma_f32_16x16x128_f8f6f4 v[90:93], v[10:17], v[190:197], v[90:93]
	v_mfma_f32_16x16x128_f8f6f4 v[78:81], v[2:9], v[218:225], v[78:81]
	v_mfma_f32_16x16x128_f8f6f4 v[74:77], v[10:17], v[218:225], v[74:77]
	v_mfma_f32_16x16x128_f8f6f4 v[58:61], v[2:9], v[226:233], v[58:61]
	v_mfma_f32_16x16x128_f8f6f4 v[42:45], v[10:17], v[226:233], v[42:45]
	v_mfma_f32_16x16x128_f8f6f4 v[38:41], v[2:9], v[234:241], v[38:41]
	v_mfma_f32_16x16x128_f8f6f4 v[34:37], v[10:17], v[234:241], v[34:37]
	s_setprio 0
	s_setprio 1
	v_mfma_f32_16x16x128_f8f6f4 v[86:89], v[18:25], v[190:197], v[86:89]
	v_mfma_f32_16x16x128_f8f6f4 v[82:85], v[26:33], v[190:197], v[82:85]
	v_mfma_f32_16x16x128_f8f6f4 v[62:65], v[18:25], v[218:225], v[62:65]
	v_mfma_f32_16x16x128_f8f6f4 v[46:49], v[26:33], v[218:225], v[46:49]
	v_mfma_f32_16x16x128_f8f6f4 v[70:73], v[18:25], v[226:233], v[70:73]
	v_mfma_f32_16x16x128_f8f6f4 v[66:69], v[26:33], v[226:233], v[66:69]
	v_mfma_f32_16x16x128_f8f6f4 v[54:57], v[18:25], v[234:241], v[54:57]
	v_mfma_f32_16x16x128_f8f6f4 v[50:53], v[26:33], v[234:241], v[50:53]
	s_setprio 0
	s_barrier
	s_add_i32 s14, s14, 2
	s_cmp_gt_u32 s14, 5
	s_mov_b64 s[88:89], s[84:85]
	s_cbranch_scc0 .LBB0_619
	s_cmpk_lt_u32 s3, 0x100
	s_cbranch_scc0 .LBB0_622
	s_barrier

.LBB0_695:
	v_mov_b32_e32 v163, v0
	v_mov_b32_e32 v167, v0
	s_add_u32 s11, s22, 0x100
	s_waitcnt vmcnt(0)
	s_addc_u32 s93, s23, 0
	v_lshl_add_u64 v[170:171], s[88:89], 0, v[166:167]
	v_lshl_add_u64 v[172:173], s[88:89], 0, v[162:163]
	s_mov_b32 s14, -2
	s_mov_b64 s[96:97], 0
	v_add_u32_e32 v2, s45, v223
	v_add_u32_e32 v14, s50, v223
	s_add_u32 s22, s96, 0x100
	ds_read_b128 v[18:21], v2
	ds_read_b128 v[22:25], v2 offset:1024
	ds_read_b128 v[26:29], v2 offset:2048
	ds_read_b128 v[30:33], v2 offset:3072
	ds_read_b128 v[2:5], v14
	ds_read_b128 v[6:9], v14 offset:1024
	ds_read_b128 v[10:13], v14 offset:2048
	ds_read_b128 v[14:17], v14 offset:3072
	s_addc_u32 s23, s97, 0
	s_add_u32 s15, s11, s96
	s_addc_u32 s94, s93, s97
	s_cmpk_eq_i32 s96, 0x300
	s_cselect_b64 vcc, -1, 0
	s_and_b64 s[62:63], vcc, exec
	v_cndmask_b32_e32 v180, v164, v226, vcc
	v_cndmask_b32_e32 v178, v168, v227, vcc
	v_cndmask_b32_e32 v163, v162, v228, vcc
	v_cndmask_b32_e32 v165, v166, v229, vcc
	s_cselect_b32 s95, s7, s94
	s_cselect_b32 s94, s6, s15
	s_cselect_b32 s15, 0, s22
	v_lshl_add_u64 v[174:175], v[172:173], 0, s[96:97]
	s_add_i32 m0, s54, 0xc000
	ds_read_b128 v[192:195], v225
	ds_read_b128 v[196:199], v225 offset:1024
	ds_read_b128 v[200:203], v225 offset:2048
	ds_read_b128 v[204:207], v225 offset:3072
	ds_read_b128 v[230:233], v225 offset:4096
	ds_read_b128 v[234:237], v225 offset:5120
	ds_read_b128 v[238:241], v225 offset:6144
	ds_read_b128 v[242:245], v225 offset:7168
	global_load_lds_dwordx4 v[174:175], off
	v_lshl_add_u64 v[174:175], v[170:171], 0, s[96:97]
	s_add_i32 m0, s54, 0xe000
	s_nop 0
	global_load_lds_dwordx4 v[174:175], off
	s_waitcnt vmcnt(8)
	s_waitcnt lgkmcnt(0)
	s_barrier
	s_setprio 1
	s_waitcnt lgkmcnt(0)
	v_mfma_f32_16x16x128_f8f6f4 v[158:161], v[18:25], v[192:199], 0
	v_mfma_f32_16x16x128_f8f6f4 v[154:157], v[26:33], v[192:199], 0
	v_mfma_f32_16x16x128_f8f6f4 v[142:145], v[18:25], v[200:207], 0
	v_mfma_f32_16x16x128_f8f6f4 v[138:141], v[26:33], v[200:207], 0
	v_mfma_f32_16x16x128_f8f6f4 v[126:129], v[18:25], v[230:237], 0
	v_mfma_f32_16x16x128_f8f6f4 v[122:125], v[26:33], v[230:237], 0
	v_mfma_f32_16x16x128_f8f6f4 v[110:113], v[18:25], v[238:245], 0
	v_mfma_f32_16x16x128_f8f6f4 v[106:109], v[26:33], v[238:245], 0
	s_setprio 0
	s_setprio 1
	v_mfma_f32_16x16x128_f8f6f4 v[150:153], v[2:9], v[192:199], 0
	v_mfma_f32_16x16x128_f8f6f4 v[146:149], v[10:17], v[192:199], 0
	v_mfma_f32_16x16x128_f8f6f4 v[134:137], v[2:9], v[200:207], 0
	v_mfma_f32_16x16x128_f8f6f4 v[130:133], v[10:17], v[200:207], 0
	v_mfma_f32_16x16x128_f8f6f4 v[118:121], v[2:9], v[230:237], 0
	v_mfma_f32_16x16x128_f8f6f4 v[114:117], v[10:17], v[230:237], 0
	v_mfma_f32_16x16x128_f8f6f4 v[102:105], v[2:9], v[238:245], 0
	v_mfma_f32_16x16x128_f8f6f4 v[98:101], v[10:17], v[238:245], 0
	s_setprio 0
	s_barrier
	s_mov_b32 m0, s48
	v_lshl_add_u64 v[174:175], s[94:95], 0, v[186:187]
	s_add_u32 s62, s94, 0x20000
	ds_read_b128 v[192:195], v225 offset:16384
	ds_read_b128 v[196:199], v225 offset:17408
	ds_read_b128 v[200:203], v225 offset:18432
	ds_read_b128 v[204:207], v225 offset:19456
	ds_read_b128 v[230:233], v225 offset:20480
	ds_read_b128 v[234:237], v225 offset:21504
	ds_read_b128 v[238:241], v225 offset:22528
	ds_read_b128 v[242:245], v225 offset:23552
	global_load_lds_dwordx4 v[174:175], off
	v_lshl_add_u64 v[176:177], s[94:95], 0, v[188:189]
	s_mov_b32 m0, s49
	s_addc_u32 s63, s95, 0
	global_load_lds_dwordx4 v[176:177], off
	v_lshl_add_u64 v[182:183], s[62:63], 0, v[186:187]
	s_mov_b32 m0, s51
	s_add_u32 s96, s84, s15
	global_load_lds_dwordx4 v[182:183], off
	v_lshl_add_u64 v[182:183], s[62:63], 0, v[188:189]
	s_mov_b32 m0, s52
	s_addc_u32 s97, s85, 0
	global_load_lds_dwordx4 v[182:183], off
	s_mov_b32 m0, s54
	v_mov_b32_e32 v181, v0
	global_load_lds_dwordx4 v180, s[96:97]
	s_mov_b32 m0, s56
	v_mov_b32_e32 v179, v0
	global_load_lds_dwordx4 v178, s[96:97]
	s_waitcnt vmcnt(8)
	s_waitcnt lgkmcnt(0)
	v_lshl_add_u64 v[180:181], s[96:97], 0, v[180:181]
	v_lshl_add_u64 v[178:179], s[96:97], 0, v[178:179]
	s_barrier
	s_setprio 1
	s_waitcnt lgkmcnt(0)
	v_mfma_f32_16x16x128_f8f6f4 v[94:97], v[18:25], v[192:199], 0
	v_mfma_f32_16x16x128_f8f6f4 v[90:93], v[26:33], v[192:199], 0
	v_mfma_f32_16x16x128_f8f6f4 v[78:81], v[18:25], v[200:207], 0
	v_mfma_f32_16x16x128_f8f6f4 v[74:77], v[26:33], v[200:207], 0
	v_mfma_f32_16x16x128_f8f6f4 v[58:61], v[18:25], v[230:237], 0
	v_mfma_f32_16x16x128_f8f6f4 v[42:45], v[26:33], v[230:237], 0
	v_mfma_f32_16x16x128_f8f6f4 v[38:41], v[18:25], v[238:245], 0
	v_mfma_f32_16x16x128_f8f6f4 v[34:37], v[26:33], v[238:245], 0
	s_setprio 0
	s_setprio 1
	v_mfma_f32_16x16x128_f8f6f4 v[86:89], v[2:9], v[192:199], 0
	v_mfma_f32_16x16x128_f8f6f4 v[82:85], v[10:17], v[192:199], 0
	v_mfma_f32_16x16x128_f8f6f4 v[62:65], v[2:9], v[200:207], 0
	v_mfma_f32_16x16x128_f8f6f4 v[50:53], v[10:17], v[200:207], 0
	v_mfma_f32_16x16x128_f8f6f4 v[70:73], v[2:9], v[230:237], 0
	v_mfma_f32_16x16x128_f8f6f4 v[66:69], v[10:17], v[230:237], 0
	v_mfma_f32_16x16x128_f8f6f4 v[54:57], v[2:9], v[238:245], 0
	v_mfma_f32_16x16x128_f8f6f4 v[46:49], v[10:17], v[238:245], 0
	s_setprio 0
	s_barrier
	v_add_u32_e32 v14, s65, v223
	v_add_u32_e32 v30, s70, v223
	ds_read_b128 v[2:5], v14
	ds_read_b128 v[6:9], v14 offset:1024
	ds_read_b128 v[10:13], v14 offset:2048
	ds_read_b128 v[14:17], v14 offset:3072
	ds_read_b128 v[18:21], v30
	ds_read_b128 v[22:25], v30 offset:1024
	ds_read_b128 v[26:29], v30 offset:2048
	ds_read_b128 v[30:33], v30 offset:3072
	s_mov_b32 m0, s58
	ds_read_b128 v[192:195], v225 offset:32768
	ds_read_b128 v[196:199], v225 offset:33792
	ds_read_b128 v[200:203], v225 offset:34816
	ds_read_b128 v[204:207], v225 offset:35840
	ds_read_b128 v[230:233], v225 offset:36864
	ds_read_b128 v[234:237], v225 offset:37888
	ds_read_b128 v[238:241], v225 offset:38912
	ds_read_b128 v[242:245], v225 offset:39936
	global_load_lds_dwordx4 v163, s[96:97]
	s_mov_b32 m0, s59
	s_nop 0
	global_load_lds_dwordx4 v165, s[96:97]
	s_waitcnt vmcnt(8)
	s_waitcnt lgkmcnt(0)
	s_barrier
	s_setprio 1
	s_waitcnt lgkmcnt(0)
	v_mfma_f32_16x16x128_f8f6f4 v[158:161], v[2:9], v[192:199], v[158:161]
	v_mfma_f32_16x16x128_f8f6f4 v[154:157], v[10:17], v[192:199], v[154:157]
	v_mfma_f32_16x16x128_f8f6f4 v[142:145], v[2:9], v[200:207], v[142:145]
	v_mfma_f32_16x16x128_f8f6f4 v[138:141], v[10:17], v[200:207], v[138:141]
	v_mfma_f32_16x16x128_f8f6f4 v[126:129], v[2:9], v[230:237], v[126:129]
	v_mfma_f32_16x16x128_f8f6f4 v[122:125], v[10:17], v[230:237], v[122:125]
	v_mfma_f32_16x16x128_f8f6f4 v[110:113], v[2:9], v[238:245], v[110:113]
	v_mfma_f32_16x16x128_f8f6f4 v[106:109], v[10:17], v[238:245], v[106:109]
	s_setprio 0
	s_setprio 1
	v_mfma_f32_16x16x128_f8f6f4 v[150:153], v[18:25], v[192:199], v[150:153]
	v_mfma_f32_16x16x128_f8f6f4 v[146:149], v[26:33], v[192:199], v[146:149]
	v_mfma_f32_16x16x128_f8f6f4 v[134:137], v[18:25], v[200:207], v[134:137]
	v_mfma_f32_16x16x128_f8f6f4 v[130:133], v[26:33], v[200:207], v[130:133]
	v_mfma_f32_16x16x128_f8f6f4 v[118:121], v[18:25], v[230:237], v[118:121]
	v_mfma_f32_16x16x128_f8f6f4 v[114:117], v[26:33], v[230:237], v[114:117]
	v_mfma_f32_16x16x128_f8f6f4 v[102:105], v[18:25], v[238:245], v[102:105]
	v_mfma_f32_16x16x128_f8f6f4 v[98:101], v[26:33], v[238:245], v[98:101]
	s_setprio 0
	s_barrier
	s_mov_b32 m0, s66
	v_lshl_add_u64 v[174:175], v[174:175], 0, s[38:39]
	s_add_u32 s62, s94, 0x20080
	ds_read_b128 v[192:195], v225 offset:49152
	ds_read_b128 v[196:199], v225 offset:50176
	ds_read_b128 v[200:203], v225 offset:51200
	ds_read_b128 v[204:207], v225 offset:52224
	ds_read_b128 v[230:233], v225 offset:53248
	ds_read_b128 v[234:237], v225 offset:54272
	ds_read_b128 v[238:241], v225 offset:55296
	ds_read_b128 v[242:245], v225 offset:56320
	global_load_lds_dwordx4 v[174:175], off
	v_lshl_add_u64 v[174:175], v[176:177], 0, s[38:39]
	s_mov_b32 m0, s67
	s_addc_u32 s63, s95, 0
	global_load_lds_dwordx4 v[174:175], off
	v_lshl_add_u64 v[174:175], s[62:63], 0, v[186:187]
	s_mov_b32 m0, s71
	s_nop 0
	global_load_lds_dwordx4 v[174:175], off
	v_lshl_add_u64 v[174:175], s[62:63], 0, v[188:189]
	s_mov_b32 m0, s72
	s_nop 0
	global_load_lds_dwordx4 v[174:175], off
	v_lshl_add_u64 v[174:175], v[180:181], 0, s[38:39]
	s_mov_b32 m0, s68
	s_nop 0
	global_load_lds_dwordx4 v[174:175], off
	v_lshl_add_u64 v[174:175], v[178:179], 0, s[38:39]
	s_mov_b32 m0, s69
	s_nop 0
	global_load_lds_dwordx4 v[174:175], off
	s_waitcnt vmcnt(8)
	s_waitcnt lgkmcnt(0)
	s_barrier
	s_setprio 1
	s_waitcnt lgkmcnt(0)
	v_mfma_f32_16x16x128_f8f6f4 v[94:97], v[2:9], v[192:199], v[94:97]
	v_mfma_f32_16x16x128_f8f6f4 v[90:93], v[10:17], v[192:199], v[90:93]
	v_mfma_f32_16x16x128_f8f6f4 v[78:81], v[2:9], v[200:207], v[78:81]
	v_mfma_f32_16x16x128_f8f6f4 v[74:77], v[10:17], v[200:207], v[74:77]
	v_mfma_f32_16x16x128_f8f6f4 v[58:61], v[2:9], v[230:237], v[58:61]
	v_mfma_f32_16x16x128_f8f6f4 v[42:45], v[10:17], v[230:237], v[42:45]
	v_mfma_f32_16x16x128_f8f6f4 v[38:41], v[2:9], v[238:245], v[38:41]
	v_mfma_f32_16x16x128_f8f6f4 v[34:37], v[10:17], v[238:245], v[34:37]
	s_setprio 0
	s_setprio 1
	v_mfma_f32_16x16x128_f8f6f4 v[86:89], v[18:25], v[192:199], v[86:89]
	v_mfma_f32_16x16x128_f8f6f4 v[82:85], v[26:33], v[192:199], v[82:85]
	v_mfma_f32_16x16x128_f8f6f4 v[62:65], v[18:25], v[200:207], v[62:65]
	v_mfma_f32_16x16x128_f8f6f4 v[50:53], v[26:33], v[200:207], v[50:53]
	v_mfma_f32_16x16x128_f8f6f4 v[70:73], v[18:25], v[230:237], v[70:73]
	v_mfma_f32_16x16x128_f8f6f4 v[66:69], v[26:33], v[230:237], v[66:69]
	v_mfma_f32_16x16x128_f8f6f4 v[54:57], v[18:25], v[238:245], v[54:57]
	v_mfma_f32_16x16x128_f8f6f4 v[46:49], v[26:33], v[238:245], v[46:49]
	s_setprio 0
	s_barrier
	s_add_i32 s14, s14, 2
	s_cmp_gt_u32 s14, 5
	s_mov_b64 s[96:97], s[22:23]
.LBB0_696:
	v_add_u32_e32 v2, s45, v223
	v_add_u32_e32 v14, s50, v223
	s_add_u32 s22, s96, 0x100
	ds_read_b128 v[18:21], v2
	ds_read_b128 v[22:25], v2 offset:1024
	ds_read_b128 v[26:29], v2 offset:2048
	ds_read_b128 v[30:33], v2 offset:3072
	ds_read_b128 v[2:5], v14
	ds_read_b128 v[6:9], v14 offset:1024
	ds_read_b128 v[10:13], v14 offset:2048
	ds_read_b128 v[14:17], v14 offset:3072
	s_addc_u32 s23, s97, 0
	s_add_u32 s15, s11, s96
	s_addc_u32 s94, s93, s97
	s_cmpk_eq_i32 s96, 0x300
	s_cselect_b64 vcc, -1, 0
	s_and_b64 s[62:63], vcc, exec
	v_cndmask_b32_e32 v180, v164, v226, vcc
	v_cndmask_b32_e32 v178, v168, v227, vcc
	v_cndmask_b32_e32 v163, v162, v228, vcc
	v_cndmask_b32_e32 v165, v166, v229, vcc
	s_cselect_b32 s95, s7, s94
	s_cselect_b32 s94, s6, s15
	s_cselect_b32 s15, 0, s22
	v_lshl_add_u64 v[174:175], v[172:173], 0, s[96:97]
	s_add_i32 m0, s54, 0xc000
	ds_read_b128 v[192:195], v225
	ds_read_b128 v[196:199], v225 offset:1024
	ds_read_b128 v[200:203], v225 offset:2048
	ds_read_b128 v[204:207], v225 offset:3072
	ds_read_b128 v[230:233], v225 offset:4096
	ds_read_b128 v[234:237], v225 offset:5120
	ds_read_b128 v[238:241], v225 offset:6144
	ds_read_b128 v[242:245], v225 offset:7168
	global_load_lds_dwordx4 v[174:175], off
	v_lshl_add_u64 v[174:175], v[170:171], 0, s[96:97]
	s_add_i32 m0, s54, 0xe000
	s_nop 0
	global_load_lds_dwordx4 v[174:175], off
	s_waitcnt vmcnt(8)
	s_waitcnt lgkmcnt(0)
	s_barrier
	s_setprio 1
	s_waitcnt lgkmcnt(0)
	v_mfma_f32_16x16x128_f8f6f4 v[158:161], v[18:25], v[192:199], v[158:161]
	v_mfma_f32_16x16x128_f8f6f4 v[154:157], v[26:33], v[192:199], v[154:157]
	v_mfma_f32_16x16x128_f8f6f4 v[142:145], v[18:25], v[200:207], v[142:145]
	v_mfma_f32_16x16x128_f8f6f4 v[138:141], v[26:33], v[200:207], v[138:141]
	v_mfma_f32_16x16x128_f8f6f4 v[126:129], v[18:25], v[230:237], v[126:129]
	v_mfma_f32_16x16x128_f8f6f4 v[122:125], v[26:33], v[230:237], v[122:125]
	v_mfma_f32_16x16x128_f8f6f4 v[110:113], v[18:25], v[238:245], v[110:113]
	v_mfma_f32_16x16x128_f8f6f4 v[106:109], v[26:33], v[238:245], v[106:109]
	s_setprio 0
	s_setprio 1
	v_mfma_f32_16x16x128_f8f6f4 v[150:153], v[2:9], v[192:199], v[150:153]
	v_mfma_f32_16x16x128_f8f6f4 v[146:149], v[10:17], v[192:199], v[146:149]
	v_mfma_f32_16x16x128_f8f6f4 v[134:137], v[2:9], v[200:207], v[134:137]
	v_mfma_f32_16x16x128_f8f6f4 v[130:133], v[10:17], v[200:207], v[130:133]
	v_mfma_f32_16x16x128_f8f6f4 v[118:121], v[2:9], v[230:237], v[118:121]
	v_mfma_f32_16x16x128_f8f6f4 v[114:117], v[10:17], v[230:237], v[114:117]
	v_mfma_f32_16x16x128_f8f6f4 v[102:105], v[2:9], v[238:245], v[102:105]
	v_mfma_f32_16x16x128_f8f6f4 v[98:101], v[10:17], v[238:245], v[98:101]
	s_setprio 0
	s_barrier
	s_mov_b32 m0, s48
	v_lshl_add_u64 v[174:175], s[94:95], 0, v[186:187]
	s_add_u32 s62, s94, 0x20000
	ds_read_b128 v[192:195], v225 offset:16384
	ds_read_b128 v[196:199], v225 offset:17408
	ds_read_b128 v[200:203], v225 offset:18432
	ds_read_b128 v[204:207], v225 offset:19456
	ds_read_b128 v[230:233], v225 offset:20480
	ds_read_b128 v[234:237], v225 offset:21504
	ds_read_b128 v[238:241], v225 offset:22528
	ds_read_b128 v[242:245], v225 offset:23552
	global_load_lds_dwordx4 v[174:175], off
	v_lshl_add_u64 v[176:177], s[94:95], 0, v[188:189]
	s_mov_b32 m0, s49
	s_addc_u32 s63, s95, 0
	global_load_lds_dwordx4 v[176:177], off
	v_lshl_add_u64 v[182:183], s[62:63], 0, v[186:187]
	s_mov_b32 m0, s51
	s_add_u32 s96, s84, s15
	global_load_lds_dwordx4 v[182:183], off
	v_lshl_add_u64 v[182:183], s[62:63], 0, v[188:189]
	s_mov_b32 m0, s52
	s_addc_u32 s97, s85, 0
	global_load_lds_dwordx4 v[182:183], off
	s_mov_b32 m0, s54
	v_mov_b32_e32 v181, v0
	global_load_lds_dwordx4 v180, s[96:97]
	s_mov_b32 m0, s56
	v_mov_b32_e32 v179, v0
	global_load_lds_dwordx4 v178, s[96:97]
	s_waitcnt vmcnt(8)
	s_waitcnt lgkmcnt(0)
	v_lshl_add_u64 v[180:181], s[96:97], 0, v[180:181]
	v_lshl_add_u64 v[178:179], s[96:97], 0, v[178:179]
	s_barrier
	s_setprio 1
	s_waitcnt lgkmcnt(0)
	v_mfma_f32_16x16x128_f8f6f4 v[94:97], v[18:25], v[192:199], v[94:97]
	v_mfma_f32_16x16x128_f8f6f4 v[90:93], v[26:33], v[192:199], v[90:93]
	v_mfma_f32_16x16x128_f8f6f4 v[78:81], v[18:25], v[200:207], v[78:81]
	v_mfma_f32_16x16x128_f8f6f4 v[74:77], v[26:33], v[200:207], v[74:77]
	v_mfma_f32_16x16x128_f8f6f4 v[58:61], v[18:25], v[230:237], v[58:61]
	v_mfma_f32_16x16x128_f8f6f4 v[42:45], v[26:33], v[230:237], v[42:45]
	v_mfma_f32_16x16x128_f8f6f4 v[38:41], v[18:25], v[238:245], v[38:41]
	v_mfma_f32_16x16x128_f8f6f4 v[34:37], v[26:33], v[238:245], v[34:37]
	s_setprio 0
	s_setprio 1
	v_mfma_f32_16x16x128_f8f6f4 v[86:89], v[2:9], v[192:199], v[86:89]
	v_mfma_f32_16x16x128_f8f6f4 v[82:85], v[10:17], v[192:199], v[82:85]
	v_mfma_f32_16x16x128_f8f6f4 v[62:65], v[2:9], v[200:207], v[62:65]
	v_mfma_f32_16x16x128_f8f6f4 v[50:53], v[10:17], v[200:207], v[50:53]
	v_mfma_f32_16x16x128_f8f6f4 v[70:73], v[2:9], v[230:237], v[70:73]
	v_mfma_f32_16x16x128_f8f6f4 v[66:69], v[10:17], v[230:237], v[66:69]
	v_mfma_f32_16x16x128_f8f6f4 v[54:57], v[2:9], v[238:245], v[54:57]
	v_mfma_f32_16x16x128_f8f6f4 v[46:49], v[10:17], v[238:245], v[46:49]
	s_setprio 0
	s_barrier
	v_add_u32_e32 v14, s65, v223
	v_add_u32_e32 v30, s70, v223
	ds_read_b128 v[2:5], v14
	ds_read_b128 v[6:9], v14 offset:1024
	ds_read_b128 v[10:13], v14 offset:2048
	ds_read_b128 v[14:17], v14 offset:3072
	ds_read_b128 v[18:21], v30
	ds_read_b128 v[22:25], v30 offset:1024
	ds_read_b128 v[26:29], v30 offset:2048
	ds_read_b128 v[30:33], v30 offset:3072
	s_mov_b32 m0, s58
	ds_read_b128 v[192:195], v225 offset:32768
	ds_read_b128 v[196:199], v225 offset:33792
	ds_read_b128 v[200:203], v225 offset:34816
	ds_read_b128 v[204:207], v225 offset:35840
	ds_read_b128 v[230:233], v225 offset:36864
	ds_read_b128 v[234:237], v225 offset:37888
	ds_read_b128 v[238:241], v225 offset:38912
	ds_read_b128 v[242:245], v225 offset:39936
	global_load_lds_dwordx4 v163, s[96:97]
	s_mov_b32 m0, s59
	s_nop 0
	global_load_lds_dwordx4 v165, s[96:97]
	s_waitcnt vmcnt(8)
	s_waitcnt lgkmcnt(0)
	s_barrier
	s_setprio 1
	s_waitcnt lgkmcnt(0)
	v_mfma_f32_16x16x128_f8f6f4 v[158:161], v[2:9], v[192:199], v[158:161]
	v_mfma_f32_16x16x128_f8f6f4 v[154:157], v[10:17], v[192:199], v[154:157]
	v_mfma_f32_16x16x128_f8f6f4 v[142:145], v[2:9], v[200:207], v[142:145]
	v_mfma_f32_16x16x128_f8f6f4 v[138:141], v[10:17], v[200:207], v[138:141]
	v_mfma_f32_16x16x128_f8f6f4 v[126:129], v[2:9], v[230:237], v[126:129]
	v_mfma_f32_16x16x128_f8f6f4 v[122:125], v[10:17], v[230:237], v[122:125]
	v_mfma_f32_16x16x128_f8f6f4 v[110:113], v[2:9], v[238:245], v[110:113]
	v_mfma_f32_16x16x128_f8f6f4 v[106:109], v[10:17], v[238:245], v[106:109]
	s_setprio 0
	s_setprio 1
	v_mfma_f32_16x16x128_f8f6f4 v[150:153], v[18:25], v[192:199], v[150:153]
	v_mfma_f32_16x16x128_f8f6f4 v[146:149], v[26:33], v[192:199], v[146:149]
	v_mfma_f32_16x16x128_f8f6f4 v[134:137], v[18:25], v[200:207], v[134:137]
	v_mfma_f32_16x16x128_f8f6f4 v[130:133], v[26:33], v[200:207], v[130:133]
	v_mfma_f32_16x16x128_f8f6f4 v[118:121], v[18:25], v[230:237], v[118:121]
	v_mfma_f32_16x16x128_f8f6f4 v[114:117], v[26:33], v[230:237], v[114:117]
	v_mfma_f32_16x16x128_f8f6f4 v[102:105], v[18:25], v[238:245], v[102:105]
	v_mfma_f32_16x16x128_f8f6f4 v[98:101], v[26:33], v[238:245], v[98:101]
	s_setprio 0
	s_barrier
	s_mov_b32 m0, s66
	v_lshl_add_u64 v[174:175], v[174:175], 0, s[38:39]
	s_add_u32 s62, s94, 0x20080
	ds_read_b128 v[192:195], v225 offset:49152
	ds_read_b128 v[196:199], v225 offset:50176
	ds_read_b128 v[200:203], v225 offset:51200
	ds_read_b128 v[204:207], v225 offset:52224
	ds_read_b128 v[230:233], v225 offset:53248
	ds_read_b128 v[234:237], v225 offset:54272
	ds_read_b128 v[238:241], v225 offset:55296
	ds_read_b128 v[242:245], v225 offset:56320
	global_load_lds_dwordx4 v[174:175], off
	v_lshl_add_u64 v[174:175], v[176:177], 0, s[38:39]
	s_mov_b32 m0, s67
	s_addc_u32 s63, s95, 0
	global_load_lds_dwordx4 v[174:175], off
	v_lshl_add_u64 v[174:175], s[62:63], 0, v[186:187]
	s_mov_b32 m0, s71
	s_nop 0
	global_load_lds_dwordx4 v[174:175], off
	v_lshl_add_u64 v[174:175], s[62:63], 0, v[188:189]
	s_mov_b32 m0, s72
	s_nop 0
	global_load_lds_dwordx4 v[174:175], off
	v_lshl_add_u64 v[174:175], v[180:181], 0, s[38:39]
	s_mov_b32 m0, s68
	s_nop 0
	global_load_lds_dwordx4 v[174:175], off
	v_lshl_add_u64 v[174:175], v[178:179], 0, s[38:39]
	s_mov_b32 m0, s69
	s_nop 0
	global_load_lds_dwordx4 v[174:175], off
	s_waitcnt vmcnt(8)
	s_waitcnt lgkmcnt(0)
	s_barrier
	s_setprio 1
	s_waitcnt lgkmcnt(0)
	v_mfma_f32_16x16x128_f8f6f4 v[94:97], v[2:9], v[192:199], v[94:97]
	v_mfma_f32_16x16x128_f8f6f4 v[90:93], v[10:17], v[192:199], v[90:93]
	v_mfma_f32_16x16x128_f8f6f4 v[78:81], v[2:9], v[200:207], v[78:81]
	v_mfma_f32_16x16x128_f8f6f4 v[74:77], v[10:17], v[200:207], v[74:77]
	v_mfma_f32_16x16x128_f8f6f4 v[58:61], v[2:9], v[230:237], v[58:61]
	v_mfma_f32_16x16x128_f8f6f4 v[42:45], v[10:17], v[230:237], v[42:45]
	v_mfma_f32_16x16x128_f8f6f4 v[38:41], v[2:9], v[238:245], v[38:41]
	v_mfma_f32_16x16x128_f8f6f4 v[34:37], v[10:17], v[238:245], v[34:37]
	s_setprio 0
	s_setprio 1
	v_mfma_f32_16x16x128_f8f6f4 v[86:89], v[18:25], v[192:199], v[86:89]
	v_mfma_f32_16x16x128_f8f6f4 v[82:85], v[26:33], v[192:199], v[82:85]
	v_mfma_f32_16x16x128_f8f6f4 v[62:65], v[18:25], v[200:207], v[62:65]
	v_mfma_f32_16x16x128_f8f6f4 v[50:53], v[26:33], v[200:207], v[50:53]
	v_mfma_f32_16x16x128_f8f6f4 v[70:73], v[18:25], v[230:237], v[70:73]
	v_mfma_f32_16x16x128_f8f6f4 v[66:69], v[26:33], v[230:237], v[66:69]
	v_mfma_f32_16x16x128_f8f6f4 v[54:57], v[18:25], v[238:245], v[54:57]
	v_mfma_f32_16x16x128_f8f6f4 v[46:49], v[26:33], v[238:245], v[46:49]
	s_setprio 0
	s_barrier
	s_add_i32 s14, s14, 2
	s_cmp_gt_u32 s14, 5
	s_mov_b64 s[96:97], s[22:23]
	s_cbranch_scc0 .LBB0_696
	s_and_b64 vcc, exec, s[90:91]
	s_cbranch_vccz .LBB0_699
	s_barrier

.LBB0_1056:
	s_lshl_b32 s18, s18, 4
	s_ashr_i32 s19, s18, 31
	s_lshl_b64 s[18:19], s[18:19], 2
	v_mov_b32_e32 v169, v0
	v_mov_b32_e32 v171, v0
	s_add_u32 s90, s65, s18
	s_addc_u32 s91, s66, s19
	v_lshl_add_u64 v[176:177], v[2:3], 0, s[42:43]
	v_lshl_add_u64 v[178:179], s[16:17], 0, v[170:171]
	v_lshl_add_u64 v[180:181], s[16:17], 0, v[168:169]
	s_mov_b32 s23, -2
	s_mov_b64 s[94:95], 0
	s_mov_b64 s[96:97], s[94:95]
	s_add_u32 s94, s96, 0x100
	s_addc_u32 s95, s97, 0
	s_cmpk_eq_i32 s96, 0x300
	v_lshl_add_u64 v[2:3], v[176:177], 0, s[96:97]
	s_cselect_b64 vcc, -1, 0
	v_cndmask_b32_e32 v182, v2, v166, vcc
	v_add_u32_e32 v2, s26, v197
	v_add_u32_e32 v14, s45, v197
	v_cndmask_b32_e32 v183, v3, v167, vcc
	ds_read_b128 v[18:21], v2
	ds_read_b128 v[22:25], v2 offset:1024
	ds_read_b128 v[26:29], v2 offset:2048
	ds_read_b128 v[30:33], v2 offset:3072
	ds_read_b128 v[2:5], v14
	ds_read_b128 v[6:9], v14 offset:1024
	ds_read_b128 v[10:13], v14 offset:2048
	ds_read_b128 v[14:17], v14 offset:3072
	s_and_b64 s[18:19], vcc, exec
	v_cndmask_b32_e32 v190, v172, v200, vcc
	v_cndmask_b32_e32 v188, v174, v202, vcc
	v_cndmask_b32_e32 v171, v168, v201, vcc
	v_cndmask_b32_e32 v169, v170, v203, vcc
	s_cselect_b32 s18, 0, s94
	v_lshl_add_u64 v[184:185], v[180:181], 0, s[96:97]
	s_add_i32 m0, s50, 0xc000
	ds_read_b128 v[218:221], v175
	ds_read_b128 v[222:225], v175 offset:1024
	ds_read_b128 v[226:229], v175 offset:2048
	ds_read_b128 v[230:233], v175 offset:3072
	ds_read_b128 v[234:237], v175 offset:4096
	ds_read_b128 v[238:241], v175 offset:5120
	ds_read_b128 v[242:245], v175 offset:6144
	ds_read_b128 v[246:249], v175 offset:7168
	global_load_lds_dwordx4 v[184:185], off
	v_lshl_add_u64 v[184:185], v[178:179], 0, s[96:97]
	s_add_i32 m0, s50, 0xe000
	s_nop 0
	global_load_lds_dwordx4 v[184:185], off
	s_waitcnt vmcnt(8)
	s_waitcnt lgkmcnt(0)
	s_barrier
	s_setprio 1
	s_waitcnt lgkmcnt(0)
	v_mfma_f32_16x16x128_f8f6f4 v[158:161], v[18:25], v[218:225], 0
	v_mfma_f32_16x16x128_f8f6f4 v[154:157], v[26:33], v[218:225], 0
	v_mfma_f32_16x16x128_f8f6f4 v[142:145], v[18:25], v[226:233], 0
	v_mfma_f32_16x16x128_f8f6f4 v[138:141], v[26:33], v[226:233], 0
	v_mfma_f32_16x16x128_f8f6f4 v[126:129], v[18:25], v[234:241], 0
	v_mfma_f32_16x16x128_f8f6f4 v[122:125], v[26:33], v[234:241], 0
	v_mfma_f32_16x16x128_f8f6f4 v[110:113], v[18:25], v[242:249], 0
	v_mfma_f32_16x16x128_f8f6f4 v[106:109], v[26:33], v[242:249], 0
	s_setprio 0
	s_setprio 1
	v_mfma_f32_16x16x128_f8f6f4 v[150:153], v[2:9], v[218:225], 0
	v_mfma_f32_16x16x128_f8f6f4 v[146:149], v[10:17], v[218:225], 0
	v_mfma_f32_16x16x128_f8f6f4 v[134:137], v[2:9], v[226:233], 0
	v_mfma_f32_16x16x128_f8f6f4 v[130:133], v[10:17], v[226:233], 0
	v_mfma_f32_16x16x128_f8f6f4 v[118:121], v[2:9], v[234:241], 0
	v_mfma_f32_16x16x128_f8f6f4 v[114:117], v[10:17], v[234:241], 0
	v_mfma_f32_16x16x128_f8f6f4 v[102:105], v[2:9], v[242:249], 0
	v_mfma_f32_16x16x128_f8f6f4 v[98:101], v[10:17], v[242:249], 0
	s_setprio 0
	s_barrier
	s_mov_b32 m0, s27
	v_lshl_add_u64 v[184:185], v[182:183], 0, v[162:163]
	ds_read_b128 v[218:221], v175 offset:16384
	ds_read_b128 v[222:225], v175 offset:17408
	ds_read_b128 v[226:229], v175 offset:18432
	ds_read_b128 v[230:233], v175 offset:19456
	ds_read_b128 v[234:237], v175 offset:20480
	ds_read_b128 v[238:241], v175 offset:21504
	ds_read_b128 v[242:245], v175 offset:22528
	ds_read_b128 v[246:249], v175 offset:23552
	global_load_lds_dwordx4 v[184:185], off
	v_lshl_add_u64 v[186:187], v[182:183], 0, v[164:165]
	s_mov_b32 m0, s33
	v_lshl_add_u64 v[204:205], v[182:183], 0, s[36:37]
	global_load_lds_dwordx4 v[186:187], off
	v_lshl_add_u64 v[206:207], v[204:205], 0, v[162:163]
	s_mov_b32 m0, s48
	v_lshl_add_u64 v[204:205], v[204:205], 0, v[164:165]
	global_load_lds_dwordx4 v[206:207], off
	s_mov_b32 m0, s49
	s_add_u32 vcc_lo, s12, s18
	global_load_lds_dwordx4 v[204:205], off
	s_addc_u32 vcc_hi, s13, 0
	s_mov_b32 m0, s50
	v_mov_b32_e32 v191, v0
	global_load_lds_dwordx4 v190, vcc
	s_mov_b32 m0, s51
	v_mov_b32_e32 v189, v0
	global_load_lds_dwordx4 v188, vcc
	s_waitcnt vmcnt(8)
	s_waitcnt lgkmcnt(0)
	v_lshl_add_u64 v[190:191], vcc, 0, v[190:191]
	v_lshl_add_u64 v[188:189], vcc, 0, v[188:189]
	s_barrier
	s_setprio 1
	s_waitcnt lgkmcnt(0)
	v_mfma_f32_16x16x128_f8f6f4 v[94:97], v[18:25], v[218:225], 0
	v_mfma_f32_16x16x128_f8f6f4 v[90:93], v[26:33], v[218:225], 0
	v_mfma_f32_16x16x128_f8f6f4 v[78:81], v[18:25], v[226:233], 0
	v_mfma_f32_16x16x128_f8f6f4 v[74:77], v[26:33], v[226:233], 0
	v_mfma_f32_16x16x128_f8f6f4 v[50:53], v[18:25], v[234:241], 0
	v_mfma_f32_16x16x128_f8f6f4 v[42:45], v[26:33], v[234:241], 0
	v_mfma_f32_16x16x128_f8f6f4 v[38:41], v[18:25], v[242:249], 0
	v_mfma_f32_16x16x128_f8f6f4 v[34:37], v[26:33], v[242:249], 0
	s_setprio 0
	s_setprio 1
	v_mfma_f32_16x16x128_f8f6f4 v[86:89], v[2:9], v[218:225], 0
	v_mfma_f32_16x16x128_f8f6f4 v[82:85], v[10:17], v[218:225], 0
	v_mfma_f32_16x16x128_f8f6f4 v[62:65], v[2:9], v[226:233], 0
	v_mfma_f32_16x16x128_f8f6f4 v[58:61], v[10:17], v[226:233], 0
	v_mfma_f32_16x16x128_f8f6f4 v[66:69], v[2:9], v[234:241], 0
	v_mfma_f32_16x16x128_f8f6f4 v[70:73], v[10:17], v[234:241], 0
	v_mfma_f32_16x16x128_f8f6f4 v[46:49], v[2:9], v[242:249], 0
	v_mfma_f32_16x16x128_f8f6f4 v[54:57], v[10:17], v[242:249], 0
	s_setprio 0
	s_barrier
	v_add_u32_e32 v14, s56, v197
	v_add_u32_e32 v30, s69, v197
	ds_read_b128 v[2:5], v14
	ds_read_b128 v[6:9], v14 offset:1024
	ds_read_b128 v[10:13], v14 offset:2048
	ds_read_b128 v[14:17], v14 offset:3072
	ds_read_b128 v[18:21], v30
	ds_read_b128 v[22:25], v30 offset:1024
	ds_read_b128 v[26:29], v30 offset:2048
	ds_read_b128 v[30:33], v30 offset:3072
	s_mov_b32 m0, s52
	ds_read_b128 v[218:221], v175 offset:32768
	ds_read_b128 v[222:225], v175 offset:33792
	ds_read_b128 v[226:229], v175 offset:34816
	ds_read_b128 v[230:233], v175 offset:35840
	ds_read_b128 v[234:237], v175 offset:36864
	ds_read_b128 v[238:241], v175 offset:37888
	ds_read_b128 v[242:245], v175 offset:38912
	ds_read_b128 v[246:249], v175 offset:39936
	global_load_lds_dwordx4 v171, vcc
	s_mov_b32 m0, s54
	s_nop 0
	global_load_lds_dwordx4 v169, vcc
	s_waitcnt vmcnt(8)
	s_waitcnt lgkmcnt(0)
	s_barrier
	s_setprio 1
	s_waitcnt lgkmcnt(0)
	v_mfma_f32_16x16x128_f8f6f4 v[158:161], v[2:9], v[218:225], v[158:161]
	v_mfma_f32_16x16x128_f8f6f4 v[154:157], v[10:17], v[218:225], v[154:157]
	v_mfma_f32_16x16x128_f8f6f4 v[142:145], v[2:9], v[226:233], v[142:145]
	v_mfma_f32_16x16x128_f8f6f4 v[138:141], v[10:17], v[226:233], v[138:141]
	v_mfma_f32_16x16x128_f8f6f4 v[126:129], v[2:9], v[234:241], v[126:129]
	v_mfma_f32_16x16x128_f8f6f4 v[122:125], v[10:17], v[234:241], v[122:125]
	v_mfma_f32_16x16x128_f8f6f4 v[110:113], v[2:9], v[242:249], v[110:113]
	v_mfma_f32_16x16x128_f8f6f4 v[106:109], v[10:17], v[242:249], v[106:109]
	s_setprio 0
	s_setprio 1
	v_mfma_f32_16x16x128_f8f6f4 v[150:153], v[18:25], v[218:225], v[150:153]
	v_mfma_f32_16x16x128_f8f6f4 v[146:149], v[26:33], v[218:225], v[146:149]
	v_mfma_f32_16x16x128_f8f6f4 v[134:137], v[18:25], v[226:233], v[134:137]
	v_mfma_f32_16x16x128_f8f6f4 v[130:133], v[26:33], v[226:233], v[130:133]
	v_mfma_f32_16x16x128_f8f6f4 v[118:121], v[18:25], v[234:241], v[118:121]
	v_mfma_f32_16x16x128_f8f6f4 v[114:117], v[26:33], v[234:241], v[114:117]
	v_mfma_f32_16x16x128_f8f6f4 v[102:105], v[18:25], v[242:249], v[102:105]
	v_mfma_f32_16x16x128_f8f6f4 v[98:101], v[26:33], v[242:249], v[98:101]
	s_setprio 0
	s_barrier
	s_mov_b32 m0, s61
	v_lshl_add_u64 v[184:185], v[184:185], 0, s[38:39]
	ds_read_b128 v[218:221], v175 offset:49152
	ds_read_b128 v[222:225], v175 offset:50176
	ds_read_b128 v[226:229], v175 offset:51200
	ds_read_b128 v[230:233], v175 offset:52224
	ds_read_b128 v[234:237], v175 offset:53248
	ds_read_b128 v[238:241], v175 offset:54272
	ds_read_b128 v[242:245], v175 offset:55296
	ds_read_b128 v[246:249], v175 offset:56320
	global_load_lds_dwordx4 v[184:185], off
	v_lshl_add_u64 v[184:185], v[186:187], 0, s[38:39]
	s_mov_b32 m0, s64
	v_lshl_add_u64 v[182:183], v[182:183], 0, s[40:41]
	global_load_lds_dwordx4 v[184:185], off
	v_lshl_add_u64 v[184:185], v[182:183], 0, v[162:163]
	s_mov_b32 m0, s70
	v_lshl_add_u64 v[182:183], v[182:183], 0, v[164:165]
	global_load_lds_dwordx4 v[184:185], off
	s_mov_b32 m0, s71
	s_nop 0
	global_load_lds_dwordx4 v[182:183], off
	v_lshl_add_u64 v[182:183], v[190:191], 0, s[38:39]
	s_mov_b32 m0, s67
	s_nop 0
	global_load_lds_dwordx4 v[182:183], off
	v_lshl_add_u64 v[182:183], v[188:189], 0, s[38:39]
	s_mov_b32 m0, s68
	s_nop 0
	global_load_lds_dwordx4 v[182:183], off
	s_waitcnt vmcnt(8)
	s_waitcnt lgkmcnt(0)
	s_barrier
	s_setprio 1
	s_waitcnt lgkmcnt(0)
	v_mfma_f32_16x16x128_f8f6f4 v[94:97], v[2:9], v[218:225], v[94:97]
	v_mfma_f32_16x16x128_f8f6f4 v[90:93], v[10:17], v[218:225], v[90:93]
	v_mfma_f32_16x16x128_f8f6f4 v[78:81], v[2:9], v[226:233], v[78:81]
	v_mfma_f32_16x16x128_f8f6f4 v[74:77], v[10:17], v[226:233], v[74:77]
	v_mfma_f32_16x16x128_f8f6f4 v[50:53], v[2:9], v[234:241], v[50:53]
	v_mfma_f32_16x16x128_f8f6f4 v[42:45], v[10:17], v[234:241], v[42:45]
	v_mfma_f32_16x16x128_f8f6f4 v[38:41], v[2:9], v[242:249], v[38:41]
	v_mfma_f32_16x16x128_f8f6f4 v[34:37], v[10:17], v[242:249], v[34:37]
	s_setprio 0
	s_setprio 1
	v_mfma_f32_16x16x128_f8f6f4 v[86:89], v[18:25], v[218:225], v[86:89]
	v_mfma_f32_16x16x128_f8f6f4 v[82:85], v[26:33], v[218:225], v[82:85]
	v_mfma_f32_16x16x128_f8f6f4 v[62:65], v[18:25], v[226:233], v[62:65]
	v_mfma_f32_16x16x128_f8f6f4 v[58:61], v[26:33], v[226:233], v[58:61]
	v_mfma_f32_16x16x128_f8f6f4 v[66:69], v[18:25], v[234:241], v[66:69]
	v_mfma_f32_16x16x128_f8f6f4 v[70:73], v[26:33], v[234:241], v[70:73]
	v_mfma_f32_16x16x128_f8f6f4 v[46:49], v[18:25], v[242:249], v[46:49]
	v_mfma_f32_16x16x128_f8f6f4 v[54:57], v[26:33], v[242:249], v[54:57]
	s_setprio 0
	s_barrier
	s_cmp_eq_u32 s96, 0
	s_cselect_b64 s[18:19], -1, 0
	s_and_b64 s[18:19], s[18:19], s[88:89]
	s_xor_b64 s[62:63], s[18:19], -1
	s_and_b64 s[62:63], s[62:63], s[88:89]
	s_andn2_b64 s[92:93], s[92:93], exec
	s_and_b64 s[62:63], s[62:63], exec
	s_and_b64 s[18:19], s[18:19], s[0:1]
	s_or_b64 s[92:93], s[92:93], s[62:63]
	s_and_saveexec_b64 s[96:97], s[18:19]
	s_cbranch_execz .Lpe1_LBB0_1058
	s_mov_b64 s[18:19], exec
	v_mbcnt_lo_u32_b32 v2, s18, 0
	v_mbcnt_hi_u32_b32 v2, s19, v2
	v_cmp_eq_u32_e32 vcc, 0, v2
	s_and_saveexec_b64 s[88:89], vcc
	s_cbranch_execz .Lpe1_LBB0_1057
	s_bcnt1_i32_b64 s18, s[18:19]
	v_mov_b32_e32 v2, s18
	global_atomic_add v0, v2, s[90:91]
	s_branch .Lpe1_LBB0_1057

.LBB0_1059:
	s_mov_b64 s[96:97], s[94:95]
	s_add_u32 s94, s96, 0x100
	s_addc_u32 s95, s97, 0
	s_cmpk_eq_i32 s96, 0x300
	v_lshl_add_u64 v[2:3], v[176:177], 0, s[96:97]
	s_cselect_b64 vcc, -1, 0
	v_cndmask_b32_e32 v182, v2, v166, vcc
	v_add_u32_e32 v2, s26, v197
	v_add_u32_e32 v14, s45, v197
	v_cndmask_b32_e32 v183, v3, v167, vcc
	ds_read_b128 v[18:21], v2
	ds_read_b128 v[22:25], v2 offset:1024
	ds_read_b128 v[26:29], v2 offset:2048
	ds_read_b128 v[30:33], v2 offset:3072
	ds_read_b128 v[2:5], v14
	ds_read_b128 v[6:9], v14 offset:1024
	ds_read_b128 v[10:13], v14 offset:2048
	ds_read_b128 v[14:17], v14 offset:3072
	s_and_b64 s[18:19], vcc, exec
	v_cndmask_b32_e32 v190, v172, v200, vcc
	v_cndmask_b32_e32 v188, v174, v202, vcc
	v_cndmask_b32_e32 v171, v168, v201, vcc
	v_cndmask_b32_e32 v169, v170, v203, vcc
	s_cselect_b32 s18, 0, s94
	v_lshl_add_u64 v[184:185], v[180:181], 0, s[96:97]
	s_add_i32 m0, s50, 0xc000
	ds_read_b128 v[218:221], v175
	ds_read_b128 v[222:225], v175 offset:1024
	ds_read_b128 v[226:229], v175 offset:2048
	ds_read_b128 v[230:233], v175 offset:3072
	ds_read_b128 v[234:237], v175 offset:4096
	ds_read_b128 v[238:241], v175 offset:5120
	ds_read_b128 v[242:245], v175 offset:6144
	ds_read_b128 v[246:249], v175 offset:7168
	global_load_lds_dwordx4 v[184:185], off
	v_lshl_add_u64 v[184:185], v[178:179], 0, s[96:97]
	s_add_i32 m0, s50, 0xe000
	s_nop 0
	global_load_lds_dwordx4 v[184:185], off
	s_waitcnt vmcnt(8)
	s_waitcnt lgkmcnt(0)
	s_barrier
	s_setprio 1
	s_waitcnt lgkmcnt(0)
	v_mfma_f32_16x16x128_f8f6f4 v[158:161], v[18:25], v[218:225], v[158:161]
	v_mfma_f32_16x16x128_f8f6f4 v[154:157], v[26:33], v[218:225], v[154:157]
	v_mfma_f32_16x16x128_f8f6f4 v[142:145], v[18:25], v[226:233], v[142:145]
	v_mfma_f32_16x16x128_f8f6f4 v[138:141], v[26:33], v[226:233], v[138:141]
	v_mfma_f32_16x16x128_f8f6f4 v[126:129], v[18:25], v[234:241], v[126:129]
	v_mfma_f32_16x16x128_f8f6f4 v[122:125], v[26:33], v[234:241], v[122:125]
	v_mfma_f32_16x16x128_f8f6f4 v[110:113], v[18:25], v[242:249], v[110:113]
	v_mfma_f32_16x16x128_f8f6f4 v[106:109], v[26:33], v[242:249], v[106:109]
	s_setprio 0
	s_setprio 1
	v_mfma_f32_16x16x128_f8f6f4 v[150:153], v[2:9], v[218:225], v[150:153]
	v_mfma_f32_16x16x128_f8f6f4 v[146:149], v[10:17], v[218:225], v[146:149]
	v_mfma_f32_16x16x128_f8f6f4 v[134:137], v[2:9], v[226:233], v[134:137]
	v_mfma_f32_16x16x128_f8f6f4 v[130:133], v[10:17], v[226:233], v[130:133]
	v_mfma_f32_16x16x128_f8f6f4 v[118:121], v[2:9], v[234:241], v[118:121]
	v_mfma_f32_16x16x128_f8f6f4 v[114:117], v[10:17], v[234:241], v[114:117]
	v_mfma_f32_16x16x128_f8f6f4 v[102:105], v[2:9], v[242:249], v[102:105]
	v_mfma_f32_16x16x128_f8f6f4 v[98:101], v[10:17], v[242:249], v[98:101]
	s_setprio 0
	s_barrier
	s_mov_b32 m0, s27
	v_lshl_add_u64 v[184:185], v[182:183], 0, v[162:163]
	ds_read_b128 v[218:221], v175 offset:16384
	ds_read_b128 v[222:225], v175 offset:17408
	ds_read_b128 v[226:229], v175 offset:18432
	ds_read_b128 v[230:233], v175 offset:19456
	ds_read_b128 v[234:237], v175 offset:20480
	ds_read_b128 v[238:241], v175 offset:21504
	ds_read_b128 v[242:245], v175 offset:22528
	ds_read_b128 v[246:249], v175 offset:23552
	global_load_lds_dwordx4 v[184:185], off
	v_lshl_add_u64 v[186:187], v[182:183], 0, v[164:165]
	s_mov_b32 m0, s33
	v_lshl_add_u64 v[204:205], v[182:183], 0, s[36:37]
	global_load_lds_dwordx4 v[186:187], off
	v_lshl_add_u64 v[206:207], v[204:205], 0, v[162:163]
	s_mov_b32 m0, s48
	v_lshl_add_u64 v[204:205], v[204:205], 0, v[164:165]
	global_load_lds_dwordx4 v[206:207], off
	s_mov_b32 m0, s49
	s_add_u32 vcc_lo, s12, s18
	global_load_lds_dwordx4 v[204:205], off
	s_addc_u32 vcc_hi, s13, 0
	s_mov_b32 m0, s50
	v_mov_b32_e32 v191, v0
	global_load_lds_dwordx4 v190, vcc
	s_mov_b32 m0, s51
	v_mov_b32_e32 v189, v0
	global_load_lds_dwordx4 v188, vcc
	s_waitcnt vmcnt(8)
	s_waitcnt lgkmcnt(0)
	v_lshl_add_u64 v[190:191], vcc, 0, v[190:191]
	v_lshl_add_u64 v[188:189], vcc, 0, v[188:189]
	s_barrier
	s_setprio 1
	s_waitcnt lgkmcnt(0)
	v_mfma_f32_16x16x128_f8f6f4 v[94:97], v[18:25], v[218:225], v[94:97]
	v_mfma_f32_16x16x128_f8f6f4 v[90:93], v[26:33], v[218:225], v[90:93]
	v_mfma_f32_16x16x128_f8f6f4 v[78:81], v[18:25], v[226:233], v[78:81]
	v_mfma_f32_16x16x128_f8f6f4 v[74:77], v[26:33], v[226:233], v[74:77]
	v_mfma_f32_16x16x128_f8f6f4 v[50:53], v[18:25], v[234:241], v[50:53]
	v_mfma_f32_16x16x128_f8f6f4 v[42:45], v[26:33], v[234:241], v[42:45]
	v_mfma_f32_16x16x128_f8f6f4 v[38:41], v[18:25], v[242:249], v[38:41]
	v_mfma_f32_16x16x128_f8f6f4 v[34:37], v[26:33], v[242:249], v[34:37]
	s_setprio 0
	s_setprio 1
	v_mfma_f32_16x16x128_f8f6f4 v[86:89], v[2:9], v[218:225], v[86:89]
	v_mfma_f32_16x16x128_f8f6f4 v[82:85], v[10:17], v[218:225], v[82:85]
	v_mfma_f32_16x16x128_f8f6f4 v[62:65], v[2:9], v[226:233], v[62:65]
	v_mfma_f32_16x16x128_f8f6f4 v[58:61], v[10:17], v[226:233], v[58:61]
	v_mfma_f32_16x16x128_f8f6f4 v[66:69], v[2:9], v[234:241], v[66:69]
	v_mfma_f32_16x16x128_f8f6f4 v[70:73], v[10:17], v[234:241], v[70:73]
	v_mfma_f32_16x16x128_f8f6f4 v[46:49], v[2:9], v[242:249], v[46:49]
	v_mfma_f32_16x16x128_f8f6f4 v[54:57], v[10:17], v[242:249], v[54:57]
	s_setprio 0
	s_barrier
	v_add_u32_e32 v14, s56, v197
	v_add_u32_e32 v30, s69, v197
	ds_read_b128 v[2:5], v14
	ds_read_b128 v[6:9], v14 offset:1024
	ds_read_b128 v[10:13], v14 offset:2048
	ds_read_b128 v[14:17], v14 offset:3072
	ds_read_b128 v[18:21], v30
	ds_read_b128 v[22:25], v30 offset:1024
	ds_read_b128 v[26:29], v30 offset:2048
	ds_read_b128 v[30:33], v30 offset:3072
	s_mov_b32 m0, s52
	ds_read_b128 v[218:221], v175 offset:32768
	ds_read_b128 v[222:225], v175 offset:33792
	ds_read_b128 v[226:229], v175 offset:34816
	ds_read_b128 v[230:233], v175 offset:35840
	ds_read_b128 v[234:237], v175 offset:36864
	ds_read_b128 v[238:241], v175 offset:37888
	ds_read_b128 v[242:245], v175 offset:38912
	ds_read_b128 v[246:249], v175 offset:39936
	global_load_lds_dwordx4 v171, vcc
	s_mov_b32 m0, s54
	s_nop 0
	global_load_lds_dwordx4 v169, vcc
	s_waitcnt vmcnt(8)
	s_waitcnt lgkmcnt(0)
	s_barrier
	s_setprio 1
	s_waitcnt lgkmcnt(0)
	v_mfma_f32_16x16x128_f8f6f4 v[158:161], v[2:9], v[218:225], v[158:161]
	v_mfma_f32_16x16x128_f8f6f4 v[154:157], v[10:17], v[218:225], v[154:157]
	v_mfma_f32_16x16x128_f8f6f4 v[142:145], v[2:9], v[226:233], v[142:145]
	v_mfma_f32_16x16x128_f8f6f4 v[138:141], v[10:17], v[226:233], v[138:141]
	v_mfma_f32_16x16x128_f8f6f4 v[126:129], v[2:9], v[234:241], v[126:129]
	v_mfma_f32_16x16x128_f8f6f4 v[122:125], v[10:17], v[234:241], v[122:125]
	v_mfma_f32_16x16x128_f8f6f4 v[110:113], v[2:9], v[242:249], v[110:113]
	v_mfma_f32_16x16x128_f8f6f4 v[106:109], v[10:17], v[242:249], v[106:109]
	s_setprio 0
	s_setprio 1
	v_mfma_f32_16x16x128_f8f6f4 v[150:153], v[18:25], v[218:225], v[150:153]
	v_mfma_f32_16x16x128_f8f6f4 v[146:149], v[26:33], v[218:225], v[146:149]
	v_mfma_f32_16x16x128_f8f6f4 v[134:137], v[18:25], v[226:233], v[134:137]
	v_mfma_f32_16x16x128_f8f6f4 v[130:133], v[26:33], v[226:233], v[130:133]
	v_mfma_f32_16x16x128_f8f6f4 v[118:121], v[18:25], v[234:241], v[118:121]
	v_mfma_f32_16x16x128_f8f6f4 v[114:117], v[26:33], v[234:241], v[114:117]
	v_mfma_f32_16x16x128_f8f6f4 v[102:105], v[18:25], v[242:249], v[102:105]
	v_mfma_f32_16x16x128_f8f6f4 v[98:101], v[26:33], v[242:249], v[98:101]
	s_setprio 0
	s_barrier
	s_mov_b32 m0, s61
	v_lshl_add_u64 v[184:185], v[184:185], 0, s[38:39]
	ds_read_b128 v[218:221], v175 offset:49152
	ds_read_b128 v[222:225], v175 offset:50176
	ds_read_b128 v[226:229], v175 offset:51200
	ds_read_b128 v[230:233], v175 offset:52224
	ds_read_b128 v[234:237], v175 offset:53248
	ds_read_b128 v[238:241], v175 offset:54272
	ds_read_b128 v[242:245], v175 offset:55296
	ds_read_b128 v[246:249], v175 offset:56320
	global_load_lds_dwordx4 v[184:185], off
	v_lshl_add_u64 v[184:185], v[186:187], 0, s[38:39]
	s_mov_b32 m0, s64
	v_lshl_add_u64 v[182:183], v[182:183], 0, s[40:41]
	global_load_lds_dwordx4 v[184:185], off
	v_lshl_add_u64 v[184:185], v[182:183], 0, v[162:163]
	s_mov_b32 m0, s70
	v_lshl_add_u64 v[182:183], v[182:183], 0, v[164:165]
	global_load_lds_dwordx4 v[184:185], off
	s_mov_b32 m0, s71
	s_nop 0
	global_load_lds_dwordx4 v[182:183], off
	v_lshl_add_u64 v[182:183], v[190:191], 0, s[38:39]
	s_mov_b32 m0, s67
	s_nop 0
	global_load_lds_dwordx4 v[182:183], off
	v_lshl_add_u64 v[182:183], v[188:189], 0, s[38:39]
	s_mov_b32 m0, s68
	s_nop 0
	global_load_lds_dwordx4 v[182:183], off
	s_waitcnt vmcnt(8)
	s_waitcnt lgkmcnt(0)
	s_barrier
	s_setprio 1
	s_waitcnt lgkmcnt(0)
	v_mfma_f32_16x16x128_f8f6f4 v[94:97], v[2:9], v[218:225], v[94:97]
	v_mfma_f32_16x16x128_f8f6f4 v[90:93], v[10:17], v[218:225], v[90:93]
	v_mfma_f32_16x16x128_f8f6f4 v[78:81], v[2:9], v[226:233], v[78:81]
	v_mfma_f32_16x16x128_f8f6f4 v[74:77], v[10:17], v[226:233], v[74:77]
	v_mfma_f32_16x16x128_f8f6f4 v[50:53], v[2:9], v[234:241], v[50:53]
	v_mfma_f32_16x16x128_f8f6f4 v[42:45], v[10:17], v[234:241], v[42:45]
	v_mfma_f32_16x16x128_f8f6f4 v[38:41], v[2:9], v[242:249], v[38:41]
	v_mfma_f32_16x16x128_f8f6f4 v[34:37], v[10:17], v[242:249], v[34:37]
	s_setprio 0
	s_setprio 1
	v_mfma_f32_16x16x128_f8f6f4 v[86:89], v[18:25], v[218:225], v[86:89]
	v_mfma_f32_16x16x128_f8f6f4 v[82:85], v[26:33], v[218:225], v[82:85]
	v_mfma_f32_16x16x128_f8f6f4 v[62:65], v[18:25], v[226:233], v[62:65]
	v_mfma_f32_16x16x128_f8f6f4 v[58:61], v[26:33], v[226:233], v[58:61]
	v_mfma_f32_16x16x128_f8f6f4 v[66:69], v[18:25], v[234:241], v[66:69]
	v_mfma_f32_16x16x128_f8f6f4 v[70:73], v[26:33], v[234:241], v[70:73]
	v_mfma_f32_16x16x128_f8f6f4 v[46:49], v[18:25], v[242:249], v[46:49]
	v_mfma_f32_16x16x128_f8f6f4 v[54:57], v[26:33], v[242:249], v[54:57]
	s_setprio 0
	s_barrier
	s_cmp_eq_u32 s96, 0
	s_cselect_b64 s[18:19], -1, 0
	s_and_b64 s[18:19], s[18:19], s[88:89]
	s_xor_b64 s[62:63], s[18:19], -1
	s_and_b64 s[62:63], s[62:63], s[88:89]
	s_andn2_b64 s[92:93], s[92:93], exec
	s_and_b64 s[62:63], s[62:63], exec
	s_and_b64 s[18:19], s[18:19], s[0:1]
	s_or_b64 s[92:93], s[92:93], s[62:63]
	s_and_saveexec_b64 s[96:97], s[18:19]
	s_cbranch_execz .LBB0_1058
	s_mov_b64 s[18:19], exec
	v_mbcnt_lo_u32_b32 v2, s18, 0
	v_mbcnt_hi_u32_b32 v2, s19, v2
	v_cmp_eq_u32_e32 vcc, 0, v2
	s_and_saveexec_b64 s[88:89], vcc
	s_cbranch_execz .LBB0_1057
	s_bcnt1_i32_b64 s18, s[18:19]
	v_mov_b32_e32 v2, s18
	global_atomic_add v0, v2, s[90:91]
	s_branch .LBB0_1057

.LBB0_1109:
	s_lshl_b32 s4, s3, 4
	s_ashr_i32 s5, s4, 31
	s_lshl_b64 s[4:5], s[4:5], 2
	s_add_u32 s8, s65, s4
	s_waitcnt vmcnt(0)
	v_mov_b32_e32 v183, v0
	v_mov_b32_e32 v187, v0
	s_addc_u32 s9, s66, s5
	s_mov_b32 s12, 0
	s_cmp_eq_u32 s12, 4
	s_cselect_b64 s[4:5], -1, 0
	s_and_b64 s[10:11], s[6:7], s[4:5]
	s_lshl_b32 s24, s12, 7
	v_lshl_add_u64 v[2:3], v[190:191], 0, s[24:25]
	v_lshl_add_u64 v[2:3], v[2:3], 0, s[42:43]
	v_cndmask_b32_e64 v192, v2, v180, s[4:5]
	v_add_u32_e32 v2, s18, v189
	v_add_u32_e32 v14, s27, v189
	v_cndmask_b32_e64 v193, v3, v181, s[4:5]
	ds_read_b128 v[18:21], v2
	ds_read_b128 v[22:25], v2 offset:1024
	ds_read_b128 v[26:29], v2 offset:2048
	ds_read_b128 v[30:33], v2 offset:3072
	ds_read_b128 v[2:5], v14
	ds_read_b128 v[6:9], v14 offset:1024
	ds_read_b128 v[10:13], v14 offset:2048
	ds_read_b128 v[14:17], v14 offset:3072
	s_add_i32 s13, s24, 0x100
	s_and_b64 s[10:11], s[4:5], exec
	v_cndmask_b32_e64 v196, v184, v172, s[4:5]
	v_cndmask_b32_e64 v194, v188, v174, s[4:5]
	v_cndmask_b32_e64 v175, v182, v176, s[4:5]
	v_cndmask_b32_e64 v173, v186, v178, s[4:5]
	s_cselect_b32 s10, 0, s13
	s_add_u32 s4, s84, s24
	s_addc_u32 s5, s85, 0
	v_lshl_add_u64 v[206:207], s[4:5], 0, v[182:183]
	v_lshl_add_u64 v[206:207], v[206:207], 0, s[38:39]
	s_add_i32 m0, s48, 0xc000
	ds_read_b128 v[224:227], v217
	ds_read_b128 v[228:231], v217 offset:1024
	ds_read_b128 v[232:235], v217 offset:2048
	ds_read_b128 v[236:239], v217 offset:3072
	ds_read_b128 v[240:243], v217 offset:4096
	ds_read_b128 v[244:247], v217 offset:5120
	ds_read_b128 v[198:201], v217 offset:6144
	ds_read_b128 v[202:205], v217 offset:7168
	global_load_lds_dwordx4 v[206:207], off
	v_lshl_add_u64 v[206:207], s[4:5], 0, v[186:187]
	v_lshl_add_u64 v[206:207], v[206:207], 0, s[38:39]
	s_add_i32 m0, s48, 0xe000
	s_nop 0
	global_load_lds_dwordx4 v[206:207], off
	s_waitcnt vmcnt(8)
	s_waitcnt lgkmcnt(0)
	s_barrier
	s_setprio 1
	s_waitcnt lgkmcnt(0)
	v_mfma_f32_16x16x128_f8f6f4 v[158:161], v[18:25], v[224:231], 0
	v_mfma_f32_16x16x128_f8f6f4 v[154:157], v[26:33], v[224:231], 0
	v_mfma_f32_16x16x128_f8f6f4 v[142:145], v[18:25], v[232:239], 0
	v_mfma_f32_16x16x128_f8f6f4 v[138:141], v[26:33], v[232:239], 0
	v_mfma_f32_16x16x128_f8f6f4 v[126:129], v[18:25], v[240:247], 0
	v_mfma_f32_16x16x128_f8f6f4 v[122:125], v[26:33], v[240:247], 0
	v_mfma_f32_16x16x128_f8f6f4 v[110:113], v[18:25], v[198:205], 0
	v_mfma_f32_16x16x128_f8f6f4 v[106:109], v[26:33], v[198:205], 0
	s_setprio 0
	s_setprio 1
	v_mfma_f32_16x16x128_f8f6f4 v[150:153], v[2:9], v[224:231], 0
	v_mfma_f32_16x16x128_f8f6f4 v[146:149], v[10:17], v[224:231], 0
	v_mfma_f32_16x16x128_f8f6f4 v[134:137], v[2:9], v[232:239], 0
	v_mfma_f32_16x16x128_f8f6f4 v[130:133], v[10:17], v[232:239], 0
	v_mfma_f32_16x16x128_f8f6f4 v[118:121], v[2:9], v[240:247], 0
	v_mfma_f32_16x16x128_f8f6f4 v[114:117], v[10:17], v[240:247], 0
	v_mfma_f32_16x16x128_f8f6f4 v[102:105], v[2:9], v[198:205], 0
	v_mfma_f32_16x16x128_f8f6f4 v[98:101], v[10:17], v[198:205], 0
	s_setprio 0
	s_barrier
	s_mov_b32 m0, s19
	v_lshl_add_u64 v[198:199], v[192:193], 0, v[166:167]
	ds_read_b128 v[224:227], v217 offset:16384
	ds_read_b128 v[228:231], v217 offset:17408
	ds_read_b128 v[232:235], v217 offset:18432
	ds_read_b128 v[236:239], v217 offset:19456
	ds_read_b128 v[240:243], v217 offset:20480
	ds_read_b128 v[244:247], v217 offset:21504
	ds_read_b128 v[202:205], v217 offset:22528
	ds_read_b128 v[206:209], v217 offset:23552
	global_load_lds_dwordx4 v[198:199], off
	v_lshl_add_u64 v[200:201], v[192:193], 0, v[168:169]
	s_mov_b32 m0, s26
	v_lshl_add_u64 v[214:215], v[192:193], 0, s[74:75]
	global_load_lds_dwordx4 v[200:201], off
	v_lshl_add_u64 v[248:249], v[214:215], 0, v[166:167]
	s_mov_b32 m0, s33
	v_lshl_add_u64 v[214:215], v[214:215], 0, v[168:169]
	global_load_lds_dwordx4 v[248:249], off
	s_mov_b32 m0, s45
	s_add_u32 s4, s84, s10
	global_load_lds_dwordx4 v[214:215], off
	s_addc_u32 s5, s85, 0
	s_mov_b32 m0, s48
	v_mov_b32_e32 v197, v0
	global_load_lds_dwordx4 v196, s[4:5]
	s_mov_b32 m0, s49
	v_mov_b32_e32 v195, v0
	global_load_lds_dwordx4 v194, s[4:5]
	s_waitcnt vmcnt(8)
	s_waitcnt lgkmcnt(0)
	v_lshl_add_u64 v[196:197], s[4:5], 0, v[196:197]
	v_lshl_add_u64 v[194:195], s[4:5], 0, v[194:195]
	s_barrier
	s_setprio 1
	s_waitcnt lgkmcnt(0)
	v_mfma_f32_16x16x128_f8f6f4 v[94:97], v[18:25], v[224:231], 0
	v_mfma_f32_16x16x128_f8f6f4 v[90:93], v[26:33], v[224:231], 0
	v_mfma_f32_16x16x128_f8f6f4 v[78:81], v[18:25], v[232:239], 0
	v_mfma_f32_16x16x128_f8f6f4 v[74:77], v[26:33], v[232:239], 0
	v_mfma_f32_16x16x128_f8f6f4 v[54:57], v[18:25], v[240:247], 0
	v_mfma_f32_16x16x128_f8f6f4 v[50:53], v[26:33], v[240:247], 0
	v_mfma_f32_16x16x128_f8f6f4 v[38:41], v[18:25], v[202:209], 0
	v_mfma_f32_16x16x128_f8f6f4 v[34:37], v[26:33], v[202:209], 0
	s_setprio 0
	s_setprio 1
	v_mfma_f32_16x16x128_f8f6f4 v[86:89], v[2:9], v[224:231], 0
	v_mfma_f32_16x16x128_f8f6f4 v[82:85], v[10:17], v[224:231], 0
	v_mfma_f32_16x16x128_f8f6f4 v[70:73], v[2:9], v[232:239], 0
	v_mfma_f32_16x16x128_f8f6f4 v[58:61], v[10:17], v[232:239], 0
	v_mfma_f32_16x16x128_f8f6f4 v[66:69], v[2:9], v[240:247], 0
	v_mfma_f32_16x16x128_f8f6f4 v[62:65], v[10:17], v[240:247], 0
	v_mfma_f32_16x16x128_f8f6f4 v[46:49], v[2:9], v[202:209], 0
	v_mfma_f32_16x16x128_f8f6f4 v[42:45], v[10:17], v[202:209], 0
	s_setprio 0
	s_barrier
	v_add_u32_e32 v14, s52, v189
	v_add_u32_e32 v30, s67, v189
	ds_read_b128 v[2:5], v14
	ds_read_b128 v[6:9], v14 offset:1024
	ds_read_b128 v[10:13], v14 offset:2048
	ds_read_b128 v[14:17], v14 offset:3072
	ds_read_b128 v[18:21], v30
	ds_read_b128 v[22:25], v30 offset:1024
	ds_read_b128 v[26:29], v30 offset:2048
	ds_read_b128 v[30:33], v30 offset:3072
	s_mov_b32 m0, s50
	ds_read_b128 v[202:205], v217 offset:32768
	ds_read_b128 v[206:209], v217 offset:33792
	ds_read_b128 v[224:227], v217 offset:34816
	ds_read_b128 v[228:231], v217 offset:35840
	ds_read_b128 v[232:235], v217 offset:36864
	ds_read_b128 v[236:239], v217 offset:37888
	ds_read_b128 v[240:243], v217 offset:38912
	ds_read_b128 v[244:247], v217 offset:39936
	global_load_lds_dwordx4 v175, s[4:5]
	s_mov_b32 m0, s51
	s_nop 0
	global_load_lds_dwordx4 v173, s[4:5]
	s_waitcnt vmcnt(8)
	s_waitcnt lgkmcnt(0)
	s_barrier
	s_setprio 1
	s_waitcnt lgkmcnt(0)
	v_mfma_f32_16x16x128_f8f6f4 v[158:161], v[2:9], v[202:209], v[158:161]
	v_mfma_f32_16x16x128_f8f6f4 v[154:157], v[10:17], v[202:209], v[154:157]
	v_mfma_f32_16x16x128_f8f6f4 v[142:145], v[2:9], v[224:231], v[142:145]
	v_mfma_f32_16x16x128_f8f6f4 v[138:141], v[10:17], v[224:231], v[138:141]
	v_mfma_f32_16x16x128_f8f6f4 v[126:129], v[2:9], v[232:239], v[126:129]
	v_mfma_f32_16x16x128_f8f6f4 v[122:125], v[10:17], v[232:239], v[122:125]
	v_mfma_f32_16x16x128_f8f6f4 v[110:113], v[2:9], v[240:247], v[110:113]
	v_mfma_f32_16x16x128_f8f6f4 v[106:109], v[10:17], v[240:247], v[106:109]
	s_setprio 0
	s_setprio 1
	v_mfma_f32_16x16x128_f8f6f4 v[150:153], v[18:25], v[202:209], v[150:153]
	v_mfma_f32_16x16x128_f8f6f4 v[146:149], v[26:33], v[202:209], v[146:149]
	v_mfma_f32_16x16x128_f8f6f4 v[134:137], v[18:25], v[224:231], v[134:137]
	v_mfma_f32_16x16x128_f8f6f4 v[130:133], v[26:33], v[224:231], v[130:133]
	v_mfma_f32_16x16x128_f8f6f4 v[118:121], v[18:25], v[232:239], v[118:121]
	v_mfma_f32_16x16x128_f8f6f4 v[114:117], v[26:33], v[232:239], v[114:117]
	v_mfma_f32_16x16x128_f8f6f4 v[102:105], v[18:25], v[240:247], v[102:105]
	v_mfma_f32_16x16x128_f8f6f4 v[98:101], v[26:33], v[240:247], v[98:101]
	s_setprio 0
	s_barrier
	s_mov_b32 m0, s54
	v_lshl_add_u64 v[198:199], v[198:199], 0, s[38:39]
	ds_read_b128 v[202:205], v217 offset:49152
	ds_read_b128 v[206:209], v217 offset:50176
	ds_read_b128 v[224:227], v217 offset:51200
	ds_read_b128 v[228:231], v217 offset:52224
	ds_read_b128 v[232:235], v217 offset:53248
	ds_read_b128 v[236:239], v217 offset:54272
	ds_read_b128 v[240:243], v217 offset:55296
	ds_read_b128 v[244:247], v217 offset:56320
	global_load_lds_dwordx4 v[198:199], off
	v_lshl_add_u64 v[198:199], v[200:201], 0, s[38:39]
	s_mov_b32 m0, s56
	v_lshl_add_u64 v[192:193], v[192:193], 0, s[76:77]
	global_load_lds_dwordx4 v[198:199], off
	v_lshl_add_u64 v[198:199], v[192:193], 0, v[166:167]
	s_mov_b32 m0, s68
	v_lshl_add_u64 v[192:193], v[192:193], 0, v[168:169]
	global_load_lds_dwordx4 v[198:199], off
	s_mov_b32 m0, s69
	s_nop 0
	global_load_lds_dwordx4 v[192:193], off
	v_lshl_add_u64 v[192:193], v[196:197], 0, s[38:39]
	s_mov_b32 m0, s61
	s_nop 0
	global_load_lds_dwordx4 v[192:193], off
	v_lshl_add_u64 v[192:193], v[194:195], 0, s[38:39]
	s_mov_b32 m0, s64
	s_nop 0
	global_load_lds_dwordx4 v[192:193], off
	s_waitcnt vmcnt(8)
	s_waitcnt lgkmcnt(0)
	s_barrier
	s_setprio 1
	s_waitcnt lgkmcnt(0)
	v_mfma_f32_16x16x128_f8f6f4 v[94:97], v[2:9], v[202:209], v[94:97]
	v_mfma_f32_16x16x128_f8f6f4 v[90:93], v[10:17], v[202:209], v[90:93]
	v_mfma_f32_16x16x128_f8f6f4 v[78:81], v[2:9], v[224:231], v[78:81]
	v_mfma_f32_16x16x128_f8f6f4 v[74:77], v[10:17], v[224:231], v[74:77]
	v_mfma_f32_16x16x128_f8f6f4 v[54:57], v[2:9], v[232:239], v[54:57]
	v_mfma_f32_16x16x128_f8f6f4 v[50:53], v[10:17], v[232:239], v[50:53]
	v_mfma_f32_16x16x128_f8f6f4 v[38:41], v[2:9], v[240:247], v[38:41]
	v_mfma_f32_16x16x128_f8f6f4 v[34:37], v[10:17], v[240:247], v[34:37]
	s_setprio 0
	s_setprio 1
	v_mfma_f32_16x16x128_f8f6f4 v[86:89], v[18:25], v[202:209], v[86:89]
	v_mfma_f32_16x16x128_f8f6f4 v[82:85], v[26:33], v[202:209], v[82:85]
	v_mfma_f32_16x16x128_f8f6f4 v[70:73], v[18:25], v[224:231], v[70:73]
	v_mfma_f32_16x16x128_f8f6f4 v[58:61], v[26:33], v[224:231], v[58:61]
	v_mfma_f32_16x16x128_f8f6f4 v[66:69], v[18:25], v[232:239], v[66:69]
	v_mfma_f32_16x16x128_f8f6f4 v[62:65], v[26:33], v[232:239], v[62:65]
	v_mfma_f32_16x16x128_f8f6f4 v[46:49], v[18:25], v[240:247], v[46:49]
	v_mfma_f32_16x16x128_f8f6f4 v[42:45], v[26:33], v[240:247], v[42:45]
	s_setprio 0
	s_barrier
	s_add_i32 s4, s12, 2
	s_cmp_gt_u32 s12, 3
	s_mov_b32 s12, s4
	s_branch .LBB0_1112

.LBB0_1111:
	s_lshl_b32 s24, s12, 7
	v_lshl_add_u64 v[2:3], v[190:191], 0, s[24:25]
	v_lshl_add_u64 v[2:3], v[2:3], 0, s[42:43]
	v_cndmask_b32_e64 v192, v2, v180, s[4:5]
	v_add_u32_e32 v2, s18, v189
	v_add_u32_e32 v14, s27, v189
	v_cndmask_b32_e64 v193, v3, v181, s[4:5]
	ds_read_b128 v[18:21], v2
	ds_read_b128 v[22:25], v2 offset:1024
	ds_read_b128 v[26:29], v2 offset:2048
	ds_read_b128 v[30:33], v2 offset:3072
	ds_read_b128 v[2:5], v14
	ds_read_b128 v[6:9], v14 offset:1024
	ds_read_b128 v[10:13], v14 offset:2048
	ds_read_b128 v[14:17], v14 offset:3072
	s_add_i32 s13, s24, 0x100
	s_and_b64 s[10:11], s[4:5], exec
	v_cndmask_b32_e64 v196, v184, v172, s[4:5]
	v_cndmask_b32_e64 v194, v188, v174, s[4:5]
	v_cndmask_b32_e64 v175, v182, v176, s[4:5]
	v_cndmask_b32_e64 v173, v186, v178, s[4:5]
	s_cselect_b32 s10, 0, s13
	s_add_u32 s4, s84, s24
	s_addc_u32 s5, s85, 0
	v_lshl_add_u64 v[206:207], s[4:5], 0, v[182:183]
	v_lshl_add_u64 v[206:207], v[206:207], 0, s[38:39]
	s_add_i32 m0, s48, 0xc000
	ds_read_b128 v[224:227], v217
	ds_read_b128 v[228:231], v217 offset:1024
	ds_read_b128 v[232:235], v217 offset:2048
	ds_read_b128 v[236:239], v217 offset:3072
	ds_read_b128 v[240:243], v217 offset:4096
	ds_read_b128 v[244:247], v217 offset:5120
	ds_read_b128 v[198:201], v217 offset:6144
	ds_read_b128 v[202:205], v217 offset:7168
	global_load_lds_dwordx4 v[206:207], off
	v_lshl_add_u64 v[206:207], s[4:5], 0, v[186:187]
	v_lshl_add_u64 v[206:207], v[206:207], 0, s[38:39]
	s_add_i32 m0, s48, 0xe000
	s_nop 0
	global_load_lds_dwordx4 v[206:207], off
	s_waitcnt vmcnt(8)
	s_waitcnt lgkmcnt(0)
	s_barrier
	s_setprio 1
	s_waitcnt lgkmcnt(0)
	v_mfma_f32_16x16x128_f8f6f4 v[158:161], v[18:25], v[224:231], v[158:161]
	v_mfma_f32_16x16x128_f8f6f4 v[154:157], v[26:33], v[224:231], v[154:157]
	v_mfma_f32_16x16x128_f8f6f4 v[142:145], v[18:25], v[232:239], v[142:145]
	v_mfma_f32_16x16x128_f8f6f4 v[138:141], v[26:33], v[232:239], v[138:141]
	v_mfma_f32_16x16x128_f8f6f4 v[126:129], v[18:25], v[240:247], v[126:129]
	v_mfma_f32_16x16x128_f8f6f4 v[122:125], v[26:33], v[240:247], v[122:125]
	v_mfma_f32_16x16x128_f8f6f4 v[110:113], v[18:25], v[198:205], v[110:113]
	v_mfma_f32_16x16x128_f8f6f4 v[106:109], v[26:33], v[198:205], v[106:109]
	s_setprio 0
	s_setprio 1
	v_mfma_f32_16x16x128_f8f6f4 v[150:153], v[2:9], v[224:231], v[150:153]
	v_mfma_f32_16x16x128_f8f6f4 v[146:149], v[10:17], v[224:231], v[146:149]
	v_mfma_f32_16x16x128_f8f6f4 v[134:137], v[2:9], v[232:239], v[134:137]
	v_mfma_f32_16x16x128_f8f6f4 v[130:133], v[10:17], v[232:239], v[130:133]
	v_mfma_f32_16x16x128_f8f6f4 v[118:121], v[2:9], v[240:247], v[118:121]
	v_mfma_f32_16x16x128_f8f6f4 v[114:117], v[10:17], v[240:247], v[114:117]
	v_mfma_f32_16x16x128_f8f6f4 v[102:105], v[2:9], v[198:205], v[102:105]
	v_mfma_f32_16x16x128_f8f6f4 v[98:101], v[10:17], v[198:205], v[98:101]
	s_setprio 0
	s_barrier
	s_mov_b32 m0, s19
	v_lshl_add_u64 v[198:199], v[192:193], 0, v[166:167]
	ds_read_b128 v[224:227], v217 offset:16384
	ds_read_b128 v[228:231], v217 offset:17408
	ds_read_b128 v[232:235], v217 offset:18432
	ds_read_b128 v[236:239], v217 offset:19456
	ds_read_b128 v[240:243], v217 offset:20480
	ds_read_b128 v[244:247], v217 offset:21504
	ds_read_b128 v[202:205], v217 offset:22528
	ds_read_b128 v[206:209], v217 offset:23552
	global_load_lds_dwordx4 v[198:199], off
	v_lshl_add_u64 v[200:201], v[192:193], 0, v[168:169]
	s_mov_b32 m0, s26
	v_lshl_add_u64 v[214:215], v[192:193], 0, s[74:75]
	global_load_lds_dwordx4 v[200:201], off
	v_lshl_add_u64 v[248:249], v[214:215], 0, v[166:167]
	s_mov_b32 m0, s33
	v_lshl_add_u64 v[214:215], v[214:215], 0, v[168:169]
	global_load_lds_dwordx4 v[248:249], off
	s_mov_b32 m0, s45
	s_add_u32 s4, s84, s10
	global_load_lds_dwordx4 v[214:215], off
	s_addc_u32 s5, s85, 0
	s_mov_b32 m0, s48
	v_mov_b32_e32 v197, v0
	global_load_lds_dwordx4 v196, s[4:5]
	s_mov_b32 m0, s49
	v_mov_b32_e32 v195, v0
	global_load_lds_dwordx4 v194, s[4:5]
	s_waitcnt vmcnt(8)
	s_waitcnt lgkmcnt(0)
	v_lshl_add_u64 v[196:197], s[4:5], 0, v[196:197]
	v_lshl_add_u64 v[194:195], s[4:5], 0, v[194:195]
	s_barrier
	s_setprio 1
	s_waitcnt lgkmcnt(0)
	v_mfma_f32_16x16x128_f8f6f4 v[94:97], v[18:25], v[224:231], v[94:97]
	v_mfma_f32_16x16x128_f8f6f4 v[90:93], v[26:33], v[224:231], v[90:93]
	v_mfma_f32_16x16x128_f8f6f4 v[78:81], v[18:25], v[232:239], v[78:81]
	v_mfma_f32_16x16x128_f8f6f4 v[74:77], v[26:33], v[232:239], v[74:77]
	v_mfma_f32_16x16x128_f8f6f4 v[54:57], v[18:25], v[240:247], v[54:57]
	v_mfma_f32_16x16x128_f8f6f4 v[50:53], v[26:33], v[240:247], v[50:53]
	v_mfma_f32_16x16x128_f8f6f4 v[38:41], v[18:25], v[202:209], v[38:41]
	v_mfma_f32_16x16x128_f8f6f4 v[34:37], v[26:33], v[202:209], v[34:37]
	s_setprio 0
	s_setprio 1
	v_mfma_f32_16x16x128_f8f6f4 v[86:89], v[2:9], v[224:231], v[86:89]
	v_mfma_f32_16x16x128_f8f6f4 v[82:85], v[10:17], v[224:231], v[82:85]
	v_mfma_f32_16x16x128_f8f6f4 v[70:73], v[2:9], v[232:239], v[70:73]
	v_mfma_f32_16x16x128_f8f6f4 v[58:61], v[10:17], v[232:239], v[58:61]
	v_mfma_f32_16x16x128_f8f6f4 v[66:69], v[2:9], v[240:247], v[66:69]
	v_mfma_f32_16x16x128_f8f6f4 v[62:65], v[10:17], v[240:247], v[62:65]
	v_mfma_f32_16x16x128_f8f6f4 v[46:49], v[2:9], v[202:209], v[46:49]
	v_mfma_f32_16x16x128_f8f6f4 v[42:45], v[10:17], v[202:209], v[42:45]
	s_setprio 0
	s_barrier
	v_add_u32_e32 v14, s52, v189
	v_add_u32_e32 v30, s67, v189
	ds_read_b128 v[2:5], v14
	ds_read_b128 v[6:9], v14 offset:1024
	ds_read_b128 v[10:13], v14 offset:2048
	ds_read_b128 v[14:17], v14 offset:3072
	ds_read_b128 v[18:21], v30
	ds_read_b128 v[22:25], v30 offset:1024
	ds_read_b128 v[26:29], v30 offset:2048
	ds_read_b128 v[30:33], v30 offset:3072
	s_mov_b32 m0, s50
	ds_read_b128 v[202:205], v217 offset:32768
	ds_read_b128 v[206:209], v217 offset:33792
	ds_read_b128 v[224:227], v217 offset:34816
	ds_read_b128 v[228:231], v217 offset:35840
	ds_read_b128 v[232:235], v217 offset:36864
	ds_read_b128 v[236:239], v217 offset:37888
	ds_read_b128 v[240:243], v217 offset:38912
	ds_read_b128 v[244:247], v217 offset:39936
	global_load_lds_dwordx4 v175, s[4:5]
	s_mov_b32 m0, s51
	s_nop 0
	global_load_lds_dwordx4 v173, s[4:5]
	s_waitcnt vmcnt(8)
	s_waitcnt lgkmcnt(0)
	s_barrier
	s_setprio 1
	s_waitcnt lgkmcnt(0)
	v_mfma_f32_16x16x128_f8f6f4 v[158:161], v[2:9], v[202:209], v[158:161]
	v_mfma_f32_16x16x128_f8f6f4 v[154:157], v[10:17], v[202:209], v[154:157]
	v_mfma_f32_16x16x128_f8f6f4 v[142:145], v[2:9], v[224:231], v[142:145]
	v_mfma_f32_16x16x128_f8f6f4 v[138:141], v[10:17], v[224:231], v[138:141]
	v_mfma_f32_16x16x128_f8f6f4 v[126:129], v[2:9], v[232:239], v[126:129]
	v_mfma_f32_16x16x128_f8f6f4 v[122:125], v[10:17], v[232:239], v[122:125]
	v_mfma_f32_16x16x128_f8f6f4 v[110:113], v[2:9], v[240:247], v[110:113]
	v_mfma_f32_16x16x128_f8f6f4 v[106:109], v[10:17], v[240:247], v[106:109]
	s_setprio 0
	s_setprio 1
	v_mfma_f32_16x16x128_f8f6f4 v[150:153], v[18:25], v[202:209], v[150:153]
	v_mfma_f32_16x16x128_f8f6f4 v[146:149], v[26:33], v[202:209], v[146:149]
	v_mfma_f32_16x16x128_f8f6f4 v[134:137], v[18:25], v[224:231], v[134:137]
	v_mfma_f32_16x16x128_f8f6f4 v[130:133], v[26:33], v[224:231], v[130:133]
	v_mfma_f32_16x16x128_f8f6f4 v[118:121], v[18:25], v[232:239], v[118:121]
	v_mfma_f32_16x16x128_f8f6f4 v[114:117], v[26:33], v[232:239], v[114:117]
	v_mfma_f32_16x16x128_f8f6f4 v[102:105], v[18:25], v[240:247], v[102:105]
	v_mfma_f32_16x16x128_f8f6f4 v[98:101], v[26:33], v[240:247], v[98:101]
	s_setprio 0
	s_barrier
	s_mov_b32 m0, s54
	v_lshl_add_u64 v[198:199], v[198:199], 0, s[38:39]
	ds_read_b128 v[202:205], v217 offset:49152
	ds_read_b128 v[206:209], v217 offset:50176
	ds_read_b128 v[224:227], v217 offset:51200
	ds_read_b128 v[228:231], v217 offset:52224
	ds_read_b128 v[232:235], v217 offset:53248
	ds_read_b128 v[236:239], v217 offset:54272
	ds_read_b128 v[240:243], v217 offset:55296
	ds_read_b128 v[244:247], v217 offset:56320
	global_load_lds_dwordx4 v[198:199], off
	v_lshl_add_u64 v[198:199], v[200:201], 0, s[38:39]
	s_mov_b32 m0, s56
	v_lshl_add_u64 v[192:193], v[192:193], 0, s[76:77]
	global_load_lds_dwordx4 v[198:199], off
	v_lshl_add_u64 v[198:199], v[192:193], 0, v[166:167]
	s_mov_b32 m0, s68
	v_lshl_add_u64 v[192:193], v[192:193], 0, v[168:169]
	global_load_lds_dwordx4 v[198:199], off
	s_mov_b32 m0, s69
	s_nop 0
	global_load_lds_dwordx4 v[192:193], off
	v_lshl_add_u64 v[192:193], v[196:197], 0, s[38:39]
	s_mov_b32 m0, s61
	s_nop 0
	global_load_lds_dwordx4 v[192:193], off
	v_lshl_add_u64 v[192:193], v[194:195], 0, s[38:39]
	s_mov_b32 m0, s64
	s_nop 0
	global_load_lds_dwordx4 v[192:193], off
	s_waitcnt vmcnt(8)
	s_waitcnt lgkmcnt(0)
	s_barrier
	s_setprio 1
	s_waitcnt lgkmcnt(0)
	v_mfma_f32_16x16x128_f8f6f4 v[94:97], v[2:9], v[202:209], v[94:97]
	v_mfma_f32_16x16x128_f8f6f4 v[90:93], v[10:17], v[202:209], v[90:93]
	v_mfma_f32_16x16x128_f8f6f4 v[78:81], v[2:9], v[224:231], v[78:81]
	v_mfma_f32_16x16x128_f8f6f4 v[74:77], v[10:17], v[224:231], v[74:77]
	v_mfma_f32_16x16x128_f8f6f4 v[54:57], v[2:9], v[232:239], v[54:57]
	v_mfma_f32_16x16x128_f8f6f4 v[50:53], v[10:17], v[232:239], v[50:53]
	v_mfma_f32_16x16x128_f8f6f4 v[38:41], v[2:9], v[240:247], v[38:41]
	v_mfma_f32_16x16x128_f8f6f4 v[34:37], v[10:17], v[240:247], v[34:37]
	s_setprio 0
	s_setprio 1
	v_mfma_f32_16x16x128_f8f6f4 v[86:89], v[18:25], v[202:209], v[86:89]
	v_mfma_f32_16x16x128_f8f6f4 v[82:85], v[26:33], v[202:209], v[82:85]
	v_mfma_f32_16x16x128_f8f6f4 v[70:73], v[18:25], v[224:231], v[70:73]
	v_mfma_f32_16x16x128_f8f6f4 v[58:61], v[26:33], v[224:231], v[58:61]
	v_mfma_f32_16x16x128_f8f6f4 v[66:69], v[18:25], v[232:239], v[66:69]
	v_mfma_f32_16x16x128_f8f6f4 v[62:65], v[26:33], v[232:239], v[62:65]
	v_mfma_f32_16x16x128_f8f6f4 v[46:49], v[18:25], v[240:247], v[46:49]
	v_mfma_f32_16x16x128_f8f6f4 v[42:45], v[26:33], v[240:247], v[42:45]
	s_setprio 0
	s_barrier
	s_add_i32 s4, s12, 2
	s_cmp_gt_u32 s12, 3
	s_mov_b32 s12, s4
	s_cbranch_scc1 .LBB0_1123
